# c1
# speedup vs baseline: 1.0111x; 1.0111x over previous
.LBB2_74:
	s_or_b64 exec, exec, s[10:11]
	v_add_u32_e32 v6, s33, v214
	v_lshl_or_b32 v6, v6, 5, v213
	v_or3_b32 v6, v6, v190, s3
	s_lshl_b32 s33, s43, 20
	v_lshlrev_b32_e32 v209, 10, v6
	v_or_b32_e32 v212, s33, v1
	s_movk_i32 s10, 0xffc0
	v_add_f32_e32 v71, 0, v71
	v_add_f32_e32 v81, 0, v72
	v_add_f32_e32 v189, 0, v73
	v_add_f32_e32 v197, 0, v74
	v_add_f32_e32 v199, 0, v75
	v_add_f32_e32 v87, 0, v87
	v_add_f32_e32 v200, 0, v88
	v_add_f32_e32 v201, 0, v89
	v_add_f32_e32 v215, 0, v90
	v_add_f32_e32 v220, 0, v91
	v_add3_u32 v80, v212, v209, s10
	v_mfma_f32_32x32x16_f16 v[34:49], v[168:171], v[2:5], v[34:49]
	ds_read_b128 v[72:75], v205 offset:41184
	ds_read_b128 v[88:91], v207 offset:41184
	v_mfma_f32_32x32x16_f16 v[2:17], v[176:179], v[2:5], 0
	s_waitcnt lgkmcnt(3)
	v_mfma_f32_32x32x16_f16 v[34:49], v[160:163], v[184:187], v[34:49]
	v_mfma_f32_32x32x16_f16 v[2:17], v[172:175], v[184:187], v[2:17]
	v_mfma_f32_32x32x16_f16 v[34:49], v[164:167], v[180:183], v[34:49]
	v_mfma_f32_32x32x16_f16 v[2:17], v[168:171], v[180:183], v[2:17]
	ds_read_b128 v[180:183], v205 offset:44352
	ds_read_b128 v[184:187], v207 offset:44352
	s_waitcnt lgkmcnt(4)
	v_mfma_f32_32x32x16_f16 v[34:49], v[156:159], v[100:103], v[34:49]
	v_mfma_f32_32x32x16_f16 v[2:17], v[160:163], v[100:103], v[2:17]
	s_waitcnt lgkmcnt(3)
	v_mfma_f32_32x32x16_f16 v[2:17], v[164:167], v[72:75], v[2:17]
	v_add_f32_e32 v62, v201, v62
	v_add_f32_e32 v63, v215, v63
	v_add_f32_e32 v60, v87, v60
	v_add_f32_e32 v61, v200, v61
	v_max_f32_e32 v62, 0, v62
	v_max_f32_e32 v63, 0, v63
	v_max_f32_e32 v60, 0, v60
	s_waitcnt lgkmcnt(2)
	v_mfma_f32_32x32x16_f16 v[2:17], v[156:159], v[88:91], v[2:17]
	v_max_f32_e32 v61, 0, v61
	v_add_f32_e32 v28, v71, v28
	v_add_f32_e32 v29, v81, v29
	ds_read_b128 v[100:103], v205 offset:45408
	ds_read_b128 v[216:219], v207 offset:45408
	v_cvt_pk_f16_f32 v63, v62, v63
	v_cvt_pk_f16_f32 v62, v60, v61
	v_add_f32_e32 v60, v220, v64
	v_add_f32_e32 v30, v189, v30
	v_add_f32_e32 v31, v197, v31
	v_max_f32_e32 v28, 0, v28
	v_max_f32_e32 v29, 0, v29
	v_max_f32_e32 v64, 0, v60
	v_max_f32_e32 v30, 0, v30
	v_max_f32_e32 v31, 0, v31
	v_cvt_pk_f16_f32 v60, v28, v29
	v_add_f32_e32 v28, v199, v32
	v_cvt_pk_f16_f32 v61, v30, v31
	v_max_f32_e32 v30, 0, v28
	v_ashrrev_i32_e32 v81, 31, v80
	v_permlane32_swap_b32_e32 v60, v62
	v_permlane32_swap_b32_e32 v61, v63
	v_permlane32_swap_b32_e32 v30, v64
	v_lshl_add_u64 v[28:29], v[80:81], 4, s[16:17]
	global_store_dwordx4 v[28:29], v[60:63], off offset:1024 sc1
	v_cvt_pk_f16_f32 v30, v30, v64
	v_lshl_add_u64 v[28:29], v[80:81], 2, s[18:19]
	global_store_dword v[28:29], v30, off offset:256 sc1
	s_waitcnt lgkmcnt(3)
	v_mfma_f32_32x32x16_f16 v[34:49], v[136:139], v[180:183], v[34:49]
	ds_read_b128 v[72:75], v205 offset:46464
	ds_read_b128 v[180:183], v207 offset:46464
	s_waitcnt lgkmcnt(4)
	v_mfma_f32_32x32x16_f16 v[34:49], v[140:143], v[184:187], v[34:49]
	s_waitcnt lgkmcnt(3)
	v_mfma_f32_32x32x16_f16 v[34:49], v[120:123], v[100:103], v[34:49]
	ds_read_b128 v[28:31], v205 offset:47520
	ds_read_b128 v[60:63], v207 offset:47520
	v_mfma_f32_32x32x16_f16 v[2:17], v[136:139], v[100:103], v[2:17]
	s_waitcnt lgkmcnt(4)
	v_mfma_f32_32x32x16_f16 v[34:49], v[152:155], v[216:219], v[34:49]
	v_mfma_f32_32x32x16_f16 v[2:17], v[140:143], v[216:219], v[2:17]
	s_waitcnt lgkmcnt(3)
	v_mfma_f32_32x32x16_f16 v[34:49], v[148:151], v[72:75], v[34:49]
	ds_read_b128 v[88:91], v205 offset:50688
	ds_read_b128 v[100:103], v207 offset:50688
	s_mov_b64 s[10:11], s[26:27]
	s_waitcnt vmcnt(3)
	ds_write_b128 v208, v[96:99] offset:16
	s_waitcnt vmcnt(2)
	ds_write_b32 v208, v188 offset:548
	v_mfma_f32_32x32x16_f16 v[2:17], v[120:123], v[72:75], v[2:17]
	s_waitcnt lgkmcnt(6)
	v_mfma_f32_32x32x16_f16 v[34:49], v[144:147], v[180:183], v[34:49]
	v_mfma_f32_32x32x16_f16 v[2:17], v[152:155], v[180:183], v[2:17]
	s_and_saveexec_b64 s[28:29], s[4:5]
	s_andn2_b64 s[10:11], s[26:27], exec
	s_and_b64 s[30:31], s[6:7], exec
	s_or_b64 s[10:11], s[10:11], s[30:31]
	ds_write_b32 v208, v188 offset:536
	s_or_b64 exec, exec, s[28:29]
	s_and_saveexec_b64 s[28:29], s[10:11]
	ds_write_b32 v208, v188 offset:560
	s_or_b64 exec, exec, s[28:29]
	s_waitcnt lgkmcnt(5)
	v_mfma_f32_32x32x16_f16 v[2:17], v[148:151], v[28:31], v[2:17]
	ds_read_b128 v[28:31], v205 offset:51744
	ds_read_b128 v[72:75], v207 offset:51744
	s_waitcnt lgkmcnt(6)
	v_mfma_f32_32x32x16_f16 v[2:17], v[144:147], v[60:63], v[2:17]
	s_waitcnt lgkmcnt(5)
	v_mfma_f32_32x32x16_f16 v[34:49], v[132:135], v[88:91], v[34:49]
	ds_read_b128 v[96:99], v205 offset:52800
	ds_read_b128 v[88:91], v207 offset:52800
	s_waitcnt lgkmcnt(6)
	v_mfma_f32_32x32x16_f16 v[34:49], v[108:111], v[100:103], v[34:49]
	s_and_saveexec_b64 s[10:11], s[0:1]
	s_cbranch_execz .LBB2_83
	s_mov_b64 s[30:31], s[26:27]
	ds_write_b128 v210, v[92:95] offset:16
	ds_write_b32 v210, v33 offset:548
	s_and_saveexec_b64 s[28:29], s[4:5]
	s_andn2_b64 s[30:31], s[26:27], exec
	s_and_b64 s[34:35], s[6:7], exec
	s_or_b64 s[30:31], s[30:31], s[34:35]
	ds_write_b32 v210, v33 offset:536
	s_or_b64 exec, exec, s[28:29]
	s_and_b64 exec, exec, s[30:31]
	ds_write_b32 v210, v33 offset:560

.LBB2_88:
	s_or_b64 exec, exec, s[10:11]
	v_mov_b32_e32 v33, v24
	v_mov_b32_e32 v24, v25
	v_mov_b32_e32 v25, v26
	v_pk_add_f32 v[184:185], v[68:69], v[24:25]
	v_mov_b32_e32 v24, v82
	v_mov_b32_e32 v25, v70
	v_mov_b32_e32 v26, v55
	v_pk_add_f32 v[180:181], v[24:25], v[26:27]
	v_mov_b32_e32 v24, v83
	v_mov_b32_e32 v25, v84
	v_mov_b32_e32 v32, v23
	v_pk_add_f32 v[186:187], v[24:25], v[56:57]
	v_mov_b32_e32 v24, v85
	v_mov_b32_e32 v25, v86
	v_pk_add_f32 v[182:183], v[66:67], v[32:33]
	v_pk_add_f32 v[188:189], v[24:25], v[58:59]
	s_waitcnt lgkmcnt(1)
	v_mfma_f32_32x32x16_f16 v[2:17], v[116:119], v[60:63], v[2:17]
	s_waitcnt lgkmcnt(0)
	v_mfma_f32_32x32x16_f16 v[2:17], v[112:115], v[28:31], v[2:17]
	s_mul_i32 s2, s2, s40
	s_bfe_u32 s28, s42, 0x30003
	s_add_i32 s2, s2, s41
	s_lshl_b32 s10, s28, 17
	s_and_b32 s2, s2, 7
	s_add_i32 s10, s33, s10
	s_nop 5
	v_mov_b32_e32 v17, 15
	s_lshl_b32 s2, s2, 12
	v_lshlrev_b32_sdwa v17, v17, v193 dst_sel:DWORD dst_unused:UNUSED_PAD src0_sel:DWORD src1_sel:BYTE_1
	v_add_lshl_u32 v23, v192, v191, 10
	s_add_i32 s2, s2, s10
	v_add3_u32 v17, s2, v17, v23
	s_movk_i32 s10, 0xfc00
	v_add3_u32 v24, v17, v1, s10
	v_ashrrev_i32_e32 v25, 31, v24
	v_lshl_add_u64 v[26:27], v[24:25], 2, s[14:15]
	v_lshlrev_b64 v[192:193], 4, v[24:25]
	v_lshlrev_b32_e32 v23, 15, v195
	v_add_lshl_u32 v24, v196, v194, 10
	v_add3_u32 v23, s2, v23, v24
	s_mov_b32 s29, 0xffff7c00
	v_add3_u32 v24, v23, v1, s29
	s_mov_b64 s[10:11], 0x280
	v_ashrrev_i32_e32 v25, 31, v24
	v_lshl_add_u64 v[32:33], v[26:27], 0, s[10:11]
	v_lshl_add_u64 v[26:27], v[24:25], 2, s[14:15]
	v_lshlrev_b64 v[196:197], 4, v[24:25]
	v_lshlrev_b32_e32 v24, 15, v198
	v_add_lshl_u32 v25, v64, v191, 10
	v_add3_u32 v28, s2, v24, v25
	v_add3_u32 v24, v28, v1, s29
	v_add_u32_e32 v217, 0xfffffc80, v17
	s_lshl_b32 s2, s28, 7
	v_lshlrev_b32_e32 v17, 5, v214
	v_ashrrev_i32_e32 v25, 31, v24
	v_or3_b32 v17, v190, s2, v17
	v_lshl_add_u64 v[194:195], v[26:27], 0, s[10:11]
	v_lshl_add_u64 v[26:27], v[24:25], 2, s[14:15]
	v_add3_u32 v17, v17, s3, v213
	s_mov_b32 s40, 2
	v_lshl_add_u64 v[198:199], v[26:27], 0, s[10:11]
	v_lshlrev_b64 v[200:201], 4, v[24:25]
	v_add_u32_e32 v215, 0xffff7c80, v28
	v_add_u32_e32 v216, 0xffff7c80, v23
	v_lshl_add_u32 v213, v17, 10, s33
	s_mov_b64 s[10:11], 0x100
	v_mov_b32_e32 v230, 0
	v_mov_b32_e32 v231, 0
	v_mov_b32_e32 v232, 0
	v_mov_b32_e32 v233, 0
	v_mov_b32_e32 v234, 0
	v_mov_b32_e32 v235, 0
	v_mov_b32_e32 v236, 0
	v_mov_b32_e32 v237, 0
	v_mov_b32_e32 v238, 0
	v_mov_b32_e32 v239, 0
	v_mov_b32_e32 v240, 0
	v_mov_b32_e32 v241, 0
	v_mov_b32_e32 v242, 0
	v_mov_b32_e32 v243, 0
	v_mov_b32_e32 v244, 0
	s_barrier
.LBB2_89:
	ds_read_b128 v[24:27], v205
	ds_read_b128 v[72:75], v205 offset:1056
	ds_read_b128 v[28:31], v207
	ds_read_b128 v[96:99], v205 offset:2112
	ds_read_b128 v[100:103], v207 offset:1056
	ds_read_b128 v[92:95], v207 offset:2112
	s_add_i32 s40, s40, 2
	v_or_b32_e32 v17, s40, v203
	s_waitcnt lgkmcnt(5)
	v_mfma_f32_32x32x16_f16 v[56:71], v[176:179], v[24:27], 0
	v_cmp_gt_u32_e64 s[2:3], 32, v17
	s_and_b64 s[28:29], vcc, s[2:3]
	s_waitcnt lgkmcnt(3)
	v_mfma_f32_32x32x16_f16 v[56:71], v[172:175], v[28:31], v[56:71]
	s_and_saveexec_b64 s[2:3], s[28:29]
	s_cbranch_execz .LBB2_91
	v_add_u32_e32 v24, v1, v215
	v_ashrrev_i32_e32 v25, 31, v24
	v_lshl_add_u64 v[26:27], v[24:25], 4, s[12:13]
	v_lshl_add_u64 v[24:25], v[24:25], 2, s[14:15]
	global_load_dwordx4 v[232:235], v[26:27], off
	global_load_dword v230, v[24:25], off
.LBB2_91:
	s_or_b64 exec, exec, s[2:3]
	v_or_b32_e32 v17, s40, v204
	v_cmp_gt_u32_e64 s[2:3], 32, v17
	s_and_b64 s[30:31], s[22:23], s[2:3]
	s_and_saveexec_b64 s[2:3], s[30:31]
	s_cbranch_execz .LBB2_93
	v_add_u32_e32 v24, v1, v216
	v_ashrrev_i32_e32 v25, 31, v24
	v_lshl_add_u64 v[26:27], v[24:25], 4, s[12:13]
	v_lshl_add_u64 v[24:25], v[24:25], 2, s[14:15]
	global_load_dwordx4 v[236:239], v[26:27], off
	global_load_dword v231, v[24:25], off
.LBB2_93:
	s_or_b64 exec, exec, s[2:3]
	v_or_b32_e32 v17, s40, v206
	v_cmp_gt_u32_e64 s[2:3], 32, v17
	s_and_b64 s[2:3], s[24:25], s[2:3]
	s_and_saveexec_b64 s[34:35], s[2:3]
	s_cbranch_execz .LBB2_95
	v_add_u32_e32 v76, v1, v217
	v_ashrrev_i32_e32 v77, 31, v76
	v_lshl_add_u64 v[24:25], v[76:77], 4, s[12:13]
	v_lshl_add_u64 v[76:77], v[76:77], 2, s[14:15]
	global_load_dwordx4 v[240:243], v[24:25], off
	global_load_dword v244, v[76:77], off
.LBB2_95:
	s_or_b64 exec, exec, s[34:35]
	v_mfma_f32_32x32x16_f16 v[56:71], v[168:171], v[72:75], v[56:71]
	ds_read_b128 v[218:221], v205 offset:3168
	ds_read_b128 v[222:225], v207 offset:3168
	v_mfma_f32_32x32x16_f16 v[72:87], v[176:179], v[72:75], 0
	s_waitcnt lgkmcnt(3)
	v_mfma_f32_32x32x16_f16 v[56:71], v[160:163], v[100:103], v[56:71]
	v_mfma_f32_32x32x16_f16 v[72:87], v[172:175], v[100:103], v[72:87]
	v_mfma_f32_32x32x16_f16 v[56:71], v[164:167], v[96:99], v[56:71]
	v_mfma_f32_32x32x16_f16 v[72:87], v[168:171], v[96:99], v[72:87]
	ds_read_b128 v[96:99], v205 offset:6336
	ds_read_b128 v[100:103], v207 offset:6336
	s_waitcnt lgkmcnt(4)
	v_mfma_f32_32x32x16_f16 v[56:71], v[156:159], v[92:95], v[56:71]
	v_mfma_f32_32x32x16_f16 v[72:87], v[160:163], v[92:95], v[72:87]
	v_add_f32_e32 v14, v187, v14
	v_add_f32_e32 v15, v188, v15
	v_add_f32_e32 v12, v180, v12
	v_add_f32_e32 v13, v186, v13
	s_waitcnt lgkmcnt(3)
	v_mfma_f32_32x32x16_f16 v[72:87], v[164:167], v[218:221], v[72:87]
	v_max_f32_e32 v14, 0, v14
	v_max_f32_e32 v15, 0, v15
	v_max_f32_e32 v12, 0, v12
	v_max_f32_e32 v13, 0, v13
	v_cvt_pk_f16_f32 v15, v14, v15
	v_cvt_pk_f16_f32 v14, v12, v13
	v_add_f32_e32 v12, v189, v16
	v_max_f32_e32 v16, 0, v12
	v_add_f32_e32 v12, v184, v46
	v_add_f32_e32 v13, v185, v47
	v_max_f32_e32 v12, 0, v12
	v_max_f32_e32 v13, 0, v13
	v_cvt_pk_f16_f32 v13, v12, v13
	v_add_f32_e32 v12, v182, v44
	v_add_f32_e32 v44, v183, v45
	s_waitcnt lgkmcnt(2)
	v_mfma_f32_32x32x16_f16 v[72:87], v[156:159], v[222:225], v[72:87]
	v_max_f32_e32 v12, 0, v12
	v_max_f32_e32 v44, 0, v44
	v_cvt_pk_f16_f32 v12, v12, v44
	v_add_f32_e32 v44, v181, v48
	ds_read_b128 v[92:95], v205 offset:7392
	ds_read_b128 v[226:229], v207 offset:7392
	v_add_u32_e32 v48, v1, v213
	v_max_f32_e32 v55, 0, v44
	v_add_u32_e32 v44, 32, v48
	v_ashrrev_i32_e32 v45, 31, v44
	v_permlane32_swap_b32_e32 v12, v14
	v_permlane32_swap_b32_e32 v13, v15
	v_permlane32_swap_b32_e32 v55, v16
	v_lshl_add_u64 v[46:47], v[44:45], 4, s[16:17]
	global_store_dwordx4 v[46:47], v[12:15], off sc1
	s_nop 1
	v_cvt_pk_f16_f32 v14, v55, v16
	v_lshl_add_u64 v[12:13], v[44:45], 2, s[18:19]
	global_store_dword v[12:13], v14, off sc1
	s_waitcnt lgkmcnt(3)
	v_mfma_f32_32x32x16_f16 v[56:71], v[136:139], v[96:99], v[56:71]
	ds_read_b128 v[96:99], v205 offset:8448
	ds_read_b128 v[180:183], v207 offset:8448
	s_waitcnt lgkmcnt(4)
	v_mfma_f32_32x32x16_f16 v[56:71], v[140:143], v[100:103], v[56:71]
	s_waitcnt lgkmcnt(3)
	v_mfma_f32_32x32x16_f16 v[56:71], v[120:123], v[92:95], v[56:71]
	ds_read_b128 v[12:15], v205 offset:9504
	ds_read_b128 v[44:47], v207 offset:9504
	v_mfma_f32_32x32x16_f16 v[72:87], v[136:139], v[92:95], v[72:87]
	s_waitcnt lgkmcnt(4)
	v_mfma_f32_32x32x16_f16 v[56:71], v[152:155], v[226:229], v[56:71]
	v_mfma_f32_32x32x16_f16 v[72:87], v[140:143], v[226:229], v[72:87]
	s_waitcnt lgkmcnt(3)
	v_mfma_f32_32x32x16_f16 v[56:71], v[148:151], v[96:99], v[56:71]
	s_mov_b64 s[34:35], s[26:27]
	v_mfma_f32_32x32x16_f16 v[72:87], v[120:123], v[96:99], v[72:87]
	ds_read_b128 v[100:103], v205 offset:12672
	ds_read_b128 v[96:99], v207 offset:12672
	s_waitcnt vmcnt(3)
	ds_write_b128 v208, v[232:235] offset:38032
	s_waitcnt vmcnt(2)
	ds_write_b32 v208, v230 offset:38564
	s_waitcnt lgkmcnt(6)
	v_mfma_f32_32x32x16_f16 v[56:71], v[144:147], v[180:183], v[56:71]
	v_mfma_f32_32x32x16_f16 v[72:87], v[152:155], v[180:183], v[72:87]
	s_and_saveexec_b64 s[36:37], s[4:5]
	s_andn2_b64 s[34:35], s[26:27], exec
	s_and_b64 s[38:39], s[6:7], exec
	s_or_b64 s[34:35], s[34:35], s[38:39]
	ds_write_b32 v208, v230 offset:38552
	s_or_b64 exec, exec, s[36:37]
	s_and_saveexec_b64 s[36:37], s[34:35]
	ds_write_b32 v208, v230 offset:38576
	s_or_b64 exec, exec, s[36:37]
	s_waitcnt lgkmcnt(5)
	v_mfma_f32_32x32x16_f16 v[72:87], v[148:151], v[12:15], v[72:87]
	ds_read_b128 v[92:95], v205 offset:13728
	ds_read_b128 v[12:15], v207 offset:13728
	s_waitcnt lgkmcnt(6)
	v_mfma_f32_32x32x16_f16 v[72:87], v[144:147], v[44:47], v[72:87]
	s_waitcnt lgkmcnt(5)
	v_mfma_f32_32x32x16_f16 v[56:71], v[132:135], v[100:103], v[56:71]
	ds_read_b128 v[88:91], v205 offset:14784
	ds_read_b128 v[44:47], v207 offset:14784
	s_waitcnt lgkmcnt(6)
	v_mfma_f32_32x32x16_f16 v[56:71], v[108:111], v[96:99], v[56:71]
	s_and_saveexec_b64 s[34:35], s[0:1]
	s_cbranch_execz .LBB2_104
	s_mov_b64 s[38:39], s[26:27]
	ds_write_b128 v210, v[236:239] offset:38032
	ds_write_b32 v210, v231 offset:38564
	s_and_saveexec_b64 s[36:37], s[4:5]
	s_andn2_b64 s[38:39], s[26:27], exec
	s_and_b64 s[42:43], s[6:7], exec
	s_or_b64 s[38:39], s[38:39], s[42:43]
	ds_write_b32 v210, v231 offset:38552
	s_or_b64 exec, exec, s[36:37]
	s_and_b64 exec, exec, s[38:39]
	ds_write_b32 v210, v231 offset:38576
.LBB2_104:
	s_or_b64 exec, exec, s[34:35]
	s_waitcnt lgkmcnt(3)
	v_mfma_f32_32x32x16_f16 v[56:71], v[128:131], v[92:95], v[56:71]
	v_mfma_f32_32x32x16_f16 v[72:87], v[132:135], v[92:95], v[72:87]
	ds_read_b128 v[92:95], v205 offset:15840
	ds_read_b128 v[28:31], v207 offset:15840
	s_waitcnt lgkmcnt(4)
	v_mfma_f32_32x32x16_f16 v[56:71], v[124:127], v[12:15], v[56:71]
	v_mfma_f32_32x32x16_f16 v[72:87], v[108:111], v[12:15], v[72:87]
	s_waitcnt lgkmcnt(3)
	v_mfma_f32_32x32x16_f16 v[56:71], v[116:119], v[88:91], v[56:71]
	v_mfma_f32_32x32x16_f16 v[72:87], v[128:131], v[88:91], v[72:87]
	s_waitcnt lgkmcnt(2)
	v_mfma_f32_32x32x16_f16 v[56:71], v[112:115], v[44:47], v[56:71]
	v_mfma_f32_32x32x16_f16 v[72:87], v[124:127], v[44:47], v[72:87]
	s_and_saveexec_b64 s[34:35], s[8:9]
	s_cbranch_execz .LBB2_109
	s_mov_b64 s[38:39], s[26:27]
	ds_write_b128 v211, v[240:243] offset:38032
	ds_write_b32 v211, v244 offset:38564
	s_and_saveexec_b64 s[36:37], s[4:5]
	s_andn2_b64 s[38:39], s[26:27], exec
	s_and_b64 s[42:43], s[6:7], exec
	s_or_b64 s[38:39], s[38:39], s[42:43]
	ds_write_b32 v211, v244 offset:38552
	s_or_b64 exec, exec, s[36:37]
	s_and_b64 exec, exec, s[38:39]
	ds_write_b32 v211, v244 offset:38576
.LBB2_109:
	s_or_b64 exec, exec, s[34:35]
	s_waitcnt lgkmcnt(1)
	v_mfma_f32_32x32x16_f16 v[72:87], v[116:119], v[92:95], v[72:87]
	s_waitcnt lgkmcnt(0)
	v_mfma_f32_32x32x16_f16 v[72:87], v[112:115], v[28:31], v[72:87]
	s_barrier
	ds_read_b128 v[24:27], v205 offset:38016
	ds_read_b128 v[12:15], v205 offset:39072
	s_waitcnt lgkmcnt(1)
	v_mfma_f32_32x32x16_f16 v[88:103], v[176:179], v[24:27], 0
	ds_read_b128 v[24:27], v207 offset:38016
	ds_read_b128 v[184:187], v205 offset:40128
	ds_read_b128 v[188:191], v207 offset:39072
	ds_read_b128 v[180:183], v207 offset:40128
	s_waitcnt lgkmcnt(3)
	v_mfma_f32_32x32x16_f16 v[88:103], v[172:175], v[24:27], v[88:103]
	s_and_saveexec_b64 s[34:35], s[28:29]
	s_cbranch_execz .LBB2_111
	v_lshl_add_u64 v[16:17], s[20:21], 0, v[200:201]
	global_load_dwordx4 v[232:235], v[16:17], off offset:2560
	global_load_dword v230, v[198:199], off
.LBB2_111:
	s_or_b64 exec, exec, s[34:35]
	s_and_saveexec_b64 s[28:29], s[30:31]
	s_cbranch_execz .LBB2_113
	v_lshl_add_u64 v[16:17], s[20:21], 0, v[196:197]
	global_load_dwordx4 v[236:239], v[16:17], off offset:2560
	global_load_dword v231, v[194:195], off
.LBB2_113:
	s_or_b64 exec, exec, s[28:29]
	s_and_saveexec_b64 s[28:29], s[2:3]
	s_cbranch_execz .LBB2_115
	v_lshl_add_u64 v[16:17], s[20:21], 0, v[192:193]
	global_load_dwordx4 v[240:243], v[16:17], off offset:2560
	global_load_dword v244, v[32:33], off
.LBB2_115:
	s_or_b64 exec, exec, s[28:29]
	v_add_f32_e32 v49, v19, v40
	v_add_f32_e32 v55, v20, v41
	v_add_f32_e32 v54, v54, v11
	v_add_f32_e32 v39, v18, v39
	v_add_f32_e32 v222, v21, v42
	v_add_f32_e32 v223, v22, v43
	v_add_f32_e32 v7, v50, v7
	v_add_f32_e32 v224, v51, v8
	v_add_f32_e32 v225, v52, v9
	v_add_f32_e32 v226, v53, v10
	v_mfma_f32_32x32x16_f16 v[88:103], v[168:171], v[12:15], v[88:103]
	ds_read_b128 v[40:43], v205 offset:41184
	ds_read_b128 v[50:53], v207 offset:41184
	v_mfma_f32_32x32x16_f16 v[8:23], v[176:179], v[12:15], 0
	s_waitcnt lgkmcnt(3)
	v_mfma_f32_32x32x16_f16 v[88:103], v[160:163], v[188:191], v[88:103]
	v_mfma_f32_32x32x16_f16 v[8:23], v[172:175], v[188:191], v[8:23]
	v_mfma_f32_32x32x16_f16 v[88:103], v[164:167], v[184:187], v[88:103]
	v_mfma_f32_32x32x16_f16 v[8:23], v[168:171], v[184:187], v[8:23]
	ds_read_b128 v[184:187], v205 offset:44352
	ds_read_b128 v[188:191], v207 offset:44352
	s_waitcnt lgkmcnt(4)
	v_mfma_f32_32x32x16_f16 v[88:103], v[156:159], v[180:183], v[88:103]
	v_mfma_f32_32x32x16_f16 v[8:23], v[160:163], v[180:183], v[8:23]
	v_add_f32_e32 v84, v225, v84
	v_add_f32_e32 v85, v226, v85
	s_waitcnt lgkmcnt(3)
	v_mfma_f32_32x32x16_f16 v[8:23], v[164:167], v[40:43], v[8:23]
	v_add_f32_e32 v40, 0, v85
	v_max_f32_e32 v84, 0, v84
	v_max_f32_e32 v40, 0, v40
	v_cvt_pk_f16_f32 v43, v84, v40
	v_add_f32_e32 v7, v7, v82
	v_add_f32_e32 v40, v224, v83
	v_max_f32_e32 v7, 0, v7
	v_max_f32_e32 v40, 0, v40
	v_cvt_pk_f16_f32 v42, v7, v40
	v_add_f32_e32 v40, v55, v68
	v_add_f32_e32 v41, v222, v69
	v_max_f32_e32 v40, 0, v40
	v_max_f32_e32 v41, 0, v41
	s_waitcnt lgkmcnt(2)
	v_mfma_f32_32x32x16_f16 v[8:23], v[156:159], v[50:53], v[8:23]
	v_cvt_pk_f16_f32 v41, v40, v41
	v_add_f32_e32 v39, v39, v66
	v_add_f32_e32 v40, v49, v67
	v_max_f32_e32 v39, 0, v39
	v_max_f32_e32 v40, 0, v40
	ds_read_b128 v[180:183], v205 offset:45408
	ds_read_b128 v[218:221], v207 offset:45408
	v_add_f32_e32 v7, v54, v86
	v_cvt_pk_f16_f32 v40, v39, v40
	v_add_f32_e32 v39, v223, v70
	v_add_u32_e32 v48, 64, v48
	v_max_f32_e32 v7, 0, v7
	v_max_f32_e32 v39, 0, v39
	v_ashrrev_i32_e32 v49, 31, v48
	v_permlane32_swap_b32_e32 v40, v42
	v_permlane32_swap_b32_e32 v41, v43
	v_permlane32_swap_b32_e32 v39, v7
	v_lshl_add_u64 v[50:51], v[48:49], 4, s[16:17]
	global_store_dwordx4 v[50:51], v[40:43], off sc1
	v_cvt_pk_f16_f32 v7, v39, v7
	s_nop 0
	v_lshl_add_u64 v[40:41], v[48:49], 2, s[18:19]
	global_store_dword v[40:41], v7, off sc1
	s_waitcnt lgkmcnt(3)
	v_mfma_f32_32x32x16_f16 v[88:103], v[136:139], v[184:187], v[88:103]
	ds_read_b128 v[52:55], v205 offset:46464
	ds_read_b128 v[66:69], v207 offset:46464
	s_waitcnt lgkmcnt(4)
	v_mfma_f32_32x32x16_f16 v[88:103], v[140:143], v[188:191], v[88:103]
	s_waitcnt lgkmcnt(3)
	v_mfma_f32_32x32x16_f16 v[88:103], v[120:123], v[180:183], v[88:103]
	ds_read_b128 v[48:51], v205 offset:47520
	ds_read_b128 v[40:43], v207 offset:47520
	v_mfma_f32_32x32x16_f16 v[8:23], v[136:139], v[180:183], v[8:23]
	s_waitcnt lgkmcnt(4)
	v_mfma_f32_32x32x16_f16 v[88:103], v[152:155], v[218:221], v[88:103]
	v_mfma_f32_32x32x16_f16 v[8:23], v[140:143], v[218:221], v[8:23]
	s_waitcnt lgkmcnt(3)
	v_mfma_f32_32x32x16_f16 v[88:103], v[148:151], v[52:55], v[88:103]
	s_mov_b64 s[2:3], s[26:27]
	v_mfma_f32_32x32x16_f16 v[8:23], v[120:123], v[52:55], v[8:23]
	ds_read_b128 v[52:55], v205 offset:50688
	ds_read_b128 v[82:85], v207 offset:50688
	s_waitcnt vmcnt(3)
	ds_write_b128 v208, v[232:235] offset:16
	s_waitcnt vmcnt(2)
	ds_write_b32 v208, v230 offset:548
	s_waitcnt lgkmcnt(6)
	v_mfma_f32_32x32x16_f16 v[88:103], v[144:147], v[66:69], v[88:103]
	v_mfma_f32_32x32x16_f16 v[8:23], v[152:155], v[66:69], v[8:23]
	s_and_saveexec_b64 s[28:29], s[4:5]
	s_andn2_b64 s[2:3], s[26:27], exec
	s_and_b64 s[30:31], s[6:7], exec
	s_or_b64 s[2:3], s[2:3], s[30:31]
	ds_write_b32 v208, v230 offset:536
	s_or_b64 exec, exec, s[28:29]
	s_and_saveexec_b64 s[28:29], s[2:3]
	ds_write_b32 v208, v230 offset:560
	s_or_b64 exec, exec, s[28:29]
	s_waitcnt lgkmcnt(5)
	v_mfma_f32_32x32x16_f16 v[8:23], v[148:151], v[48:51], v[8:23]
	ds_read_b128 v[66:69], v205 offset:51744
	ds_read_b128 v[44:47], v207 offset:51744
	s_waitcnt lgkmcnt(6)
	v_mfma_f32_32x32x16_f16 v[8:23], v[144:147], v[40:43], v[8:23]
	s_waitcnt lgkmcnt(5)
	v_mfma_f32_32x32x16_f16 v[88:103], v[132:135], v[52:55], v[88:103]
	ds_read_b128 v[52:55], v205 offset:52800
	ds_read_b128 v[48:51], v207 offset:52800
	s_waitcnt lgkmcnt(6)
	v_mfma_f32_32x32x16_f16 v[88:103], v[108:111], v[82:85], v[88:103]
	s_and_saveexec_b64 s[2:3], s[0:1]
	s_cbranch_execz .LBB2_124
	s_mov_b64 s[30:31], s[26:27]
	ds_write_b128 v210, v[236:239] offset:16
	ds_write_b32 v210, v231 offset:548
	s_and_saveexec_b64 s[28:29], s[4:5]
	s_andn2_b64 s[30:31], s[26:27], exec
	s_and_b64 s[34:35], s[6:7], exec
	s_or_b64 s[30:31], s[30:31], s[34:35]
	ds_write_b32 v210, v231 offset:536
	s_or_b64 exec, exec, s[28:29]
	s_and_b64 exec, exec, s[30:31]
	ds_write_b32 v210, v231 offset:560
.LBB2_124:
	s_or_b64 exec, exec, s[2:3]
	s_waitcnt lgkmcnt(3)
	v_mfma_f32_32x32x16_f16 v[88:103], v[128:131], v[66:69], v[88:103]
	ds_read_b128 v[40:43], v205 offset:53856
	ds_read_b128 v[28:31], v207 offset:53856
	v_mfma_f32_32x32x16_f16 v[8:23], v[132:135], v[66:69], v[8:23]
	s_waitcnt lgkmcnt(4)
	v_mfma_f32_32x32x16_f16 v[88:103], v[124:127], v[44:47], v[88:103]
	v_mfma_f32_32x32x16_f16 v[8:23], v[108:111], v[44:47], v[8:23]
	s_waitcnt lgkmcnt(3)
	v_mfma_f32_32x32x16_f16 v[88:103], v[116:119], v[52:55], v[88:103]
	v_mfma_f32_32x32x16_f16 v[8:23], v[128:131], v[52:55], v[8:23]
	s_waitcnt lgkmcnt(2)
	v_mfma_f32_32x32x16_f16 v[88:103], v[112:115], v[48:51], v[88:103]
	v_mfma_f32_32x32x16_f16 v[8:23], v[124:127], v[48:51], v[8:23]
	s_and_saveexec_b64 s[2:3], s[8:9]
	s_cbranch_execz .LBB2_129
	s_mov_b64 s[30:31], s[26:27]
	ds_write_b128 v211, v[240:243] offset:16
	ds_write_b32 v211, v244 offset:548
	s_and_saveexec_b64 s[28:29], s[4:5]
	s_andn2_b64 s[30:31], s[26:27], exec
	s_and_b64 s[34:35], s[6:7], exec
	s_or_b64 s[30:31], s[30:31], s[34:35]
	ds_write_b32 v211, v244 offset:536
	s_or_b64 exec, exec, s[28:29]
	s_and_b64 exec, exec, s[30:31]
	ds_write_b32 v211, v244 offset:560

.LBB2_131:
	ds_read_b128 v[18:21], v205
	ds_read_b128 v[34:37], v205 offset:1056
	ds_read_b128 v[38:41], v207
	ds_read_b128 v[50:53], v205 offset:2112
	ds_read_b128 v[62:65], v207 offset:1056
	ds_read_b128 v[66:69], v207 offset:2112
	s_waitcnt lgkmcnt(5)
	v_mfma_f32_32x32x16_f16 v[18:33], v[176:179], v[18:21], 0
	s_waitcnt lgkmcnt(3)
	v_mfma_f32_32x32x16_f16 v[18:33], v[172:175], v[38:41], v[18:33]
	v_add_f32_e32 v38, v183, v99
	v_add_f32_e32 v38, 0, v38
	v_mfma_f32_32x32x16_f16 v[18:33], v[168:171], v[34:37], v[18:33]
	v_max_f32_e32 v54, 0, v38
	ds_read_b128 v[78:81], v205 offset:3168
	ds_read_b128 v[82:85], v207 offset:3168
	v_add_f32_e32 v17, v182, v98
	v_add_f32_e32 v70, v56, v93
	v_add_f32_e32 v55, v184, v100
	v_add_f32_e32 v56, v185, v101
	v_add_f32_e32 v17, 0, v17
	v_mfma_f32_32x32x16_f16 v[34:49], v[176:179], v[34:37], 0
	v_add_f32_e32 v71, v57, v94
	v_add_f32_e32 v55, 0, v55
	v_add_f32_e32 v56, 0, v56
	v_add_f32_e32 v57, v181, v102
	v_max_f32_e32 v17, 0, v17
	v_max_f32_e32 v55, 0, v55
	v_max_f32_e32 v56, 0, v56
	v_add_f32_e32 v57, 0, v57
	v_add_f32_e32 v77, v58, v95
	s_waitcnt lgkmcnt(3)
	v_mfma_f32_32x32x16_f16 v[18:33], v[160:163], v[62:65], v[18:33]
	v_add_f32_e32 v86, v59, v96
	v_max_f32_e32 v87, 0, v57
	v_add_f32_e32 v93, v60, v97
	v_cvt_pk_f16_f32 v54, v17, v54
	v_cvt_pk_f16_f32 v55, v55, v56
	v_mfma_f32_32x32x16_f16 v[34:49], v[172:175], v[62:65], v[34:49]
	v_mfma_f32_32x32x16_f16 v[18:33], v[164:167], v[50:53], v[18:33]
	v_mfma_f32_32x32x16_f16 v[34:49], v[168:171], v[50:53], v[34:49]
	ds_read_b128 v[50:53], v205 offset:6336
	ds_read_b128 v[58:61], v207 offset:6336
	s_waitcnt lgkmcnt(4)
	v_mfma_f32_32x32x16_f16 v[18:33], v[156:159], v[66:69], v[18:33]
	v_mfma_f32_32x32x16_f16 v[34:49], v[160:163], v[66:69], v[34:49]
	s_waitcnt lgkmcnt(3)
	v_mfma_f32_32x32x16_f16 v[34:49], v[164:167], v[78:81], v[34:49]
	v_add_f32_e32 v7, v72, v7
	v_add_f32_e32 v17, v73, v8
	v_add_f32_e32 v8, v187, v14
	v_add_f32_e32 v72, v74, v9
	v_add_f32_e32 v9, v188, v15
	v_add_f32_e32 v12, v180, v12
	v_add_f32_e32 v13, v186, v13
	v_add_f32_e32 v8, 0, v8
	v_add_f32_e32 v9, 0, v9
	ds_read_b128 v[62:65], v205 offset:7392
	ds_read_b128 v[66:69], v207 offset:7392
	v_add_f32_e32 v12, 0, v12
	v_add_f32_e32 v13, 0, v13
	v_max_f32_e32 v8, 0, v8
	v_max_f32_e32 v9, 0, v9
	v_add_f32_e32 v73, v75, v10
	v_add_f32_e32 v10, v189, v16
	s_movk_i32 s0, 0x3a0
	v_max_f32_e32 v12, 0, v12
	v_max_f32_e32 v13, 0, v13
	v_add_f32_e32 v10, 0, v10
	v_cvt_pk_f16_f32 v57, v8, v9
	v_add3_u32 v8, v209, v212, s0
	v_max_f32_e32 v14, 0, v10
	v_cvt_pk_f16_f32 v56, v12, v13
	v_ashrrev_i32_e32 v9, 31, v8
	v_add_f32_e32 v16, v76, v11
	v_permlane32_swap_b32_e32 v54, v56
	v_permlane32_swap_b32_e32 v55, v57
	v_permlane32_swap_b32_e32 v87, v14
	v_lshl_add_u64 v[10:11], v[8:9], 4, s[16:17]
	global_store_dwordx4 v[10:11], v[54:57], off sc1
	v_cvt_pk_f16_f32 v10, v87, v14
	v_lshl_add_u64 v[8:9], v[8:9], 2, s[18:19]
	s_waitcnt lgkmcnt(4)
	v_mfma_f32_32x32x16_f16 v[34:49], v[156:159], v[82:85], v[34:49]
	global_store_dword v[8:9], v10, off sc1
	s_waitcnt lgkmcnt(3)
	v_mfma_f32_32x32x16_f16 v[18:33], v[136:139], v[50:53], v[18:33]
	ds_read_b128 v[8:11], v205 offset:8448
	ds_read_b128 v[12:15], v207 offset:8448
	s_waitcnt lgkmcnt(4)
	v_mfma_f32_32x32x16_f16 v[18:33], v[140:143], v[58:61], v[18:33]
	s_waitcnt lgkmcnt(3)
	v_mfma_f32_32x32x16_f16 v[18:33], v[120:123], v[62:65], v[18:33]
	ds_read_b128 v[50:53], v205 offset:9504
	ds_read_b128 v[54:57], v207 offset:9504
	v_mfma_f32_32x32x16_f16 v[34:49], v[136:139], v[62:65], v[34:49]
	s_waitcnt lgkmcnt(4)
	v_mfma_f32_32x32x16_f16 v[18:33], v[152:155], v[66:69], v[18:33]
	v_mfma_f32_32x32x16_f16 v[34:49], v[140:143], v[66:69], v[34:49]
	s_waitcnt lgkmcnt(3)
	v_mfma_f32_32x32x16_f16 v[18:33], v[148:151], v[8:11], v[18:33]
	v_mfma_f32_32x32x16_f16 v[34:49], v[120:123], v[8:11], v[34:49]
	ds_read_b128 v[8:11], v205 offset:12672
	ds_read_b128 v[58:61], v207 offset:12672
	s_waitcnt lgkmcnt(4)
	v_mfma_f32_32x32x16_f16 v[18:33], v[144:147], v[12:15], v[18:33]
	v_mfma_f32_32x32x16_f16 v[34:49], v[152:155], v[12:15], v[34:49]
	s_waitcnt lgkmcnt(3)
	v_mfma_f32_32x32x16_f16 v[34:49], v[148:151], v[50:53], v[34:49]
	ds_read_b128 v[12:15], v205 offset:13728
	ds_read_b128 v[50:53], v207 offset:13728
	s_waitcnt lgkmcnt(4)
	v_mfma_f32_32x32x16_f16 v[34:49], v[144:147], v[54:57], v[34:49]
	s_waitcnt lgkmcnt(3)
	v_mfma_f32_32x32x16_f16 v[18:33], v[132:135], v[8:11], v[18:33]
	ds_read_b128 v[8:11], v205 offset:14784
	ds_read_b128 v[54:57], v207 offset:14784
	s_waitcnt lgkmcnt(4)
	v_mfma_f32_32x32x16_f16 v[18:33], v[108:111], v[58:61], v[18:33]
	s_waitcnt lgkmcnt(3)
	v_mfma_f32_32x32x16_f16 v[18:33], v[128:131], v[12:15], v[18:33]
	v_mfma_f32_32x32x16_f16 v[34:49], v[132:135], v[12:15], v[34:49]
	ds_read_b128 v[12:15], v205 offset:15840
	ds_read_b128 v[58:61], v207 offset:15840
	s_waitcnt lgkmcnt(4)
	v_mfma_f32_32x32x16_f16 v[18:33], v[124:127], v[50:53], v[18:33]
	v_mfma_f32_32x32x16_f16 v[34:49], v[108:111], v[50:53], v[34:49]
	s_waitcnt lgkmcnt(3)
	v_mfma_f32_32x32x16_f16 v[18:33], v[116:119], v[8:11], v[18:33]
	v_mfma_f32_32x32x16_f16 v[34:49], v[128:131], v[8:11], v[34:49]
	s_waitcnt lgkmcnt(2)
	v_mfma_f32_32x32x16_f16 v[18:33], v[112:115], v[54:57], v[18:33]
	v_mfma_f32_32x32x16_f16 v[34:49], v[124:127], v[54:57], v[34:49]
	s_waitcnt lgkmcnt(1)
	v_mfma_f32_32x32x16_f16 v[34:49], v[116:119], v[12:15], v[34:49]
	s_waitcnt lgkmcnt(0)
	v_mfma_f32_32x32x16_f16 v[34:49], v[112:115], v[58:61], v[34:49]
	s_nop 6
	v_add_f32_e32 v8, v70, v28
	v_add_f32_e32 v9, v71, v29
	v_add_f32_e32 v10, v77, v30
	v_add_f32_e32 v11, v86, v31
	s_nop 0
	v_add_f32_e32 v7, v7, v44
	v_add_f32_e32 v20, v2, v39
	v_add_f32_e32 v2, v17, v45
	v_add_f32_e32 v8, 0, v8
	v_add_f32_e32 v9, 0, v9
	v_add_f32_e32 v10, 0, v10
	v_add_f32_e32 v11, 0, v11
	v_add_f32_e32 v7, 0, v7
	v_add_f32_e32 v2, 0, v2
	v_max_f32_e32 v8, 0, v8
	v_max_f32_e32 v9, 0, v9
	v_max_f32_e32 v10, 0, v10
	v_max_f32_e32 v11, 0, v11
	v_max_f32_e32 v7, 0, v7
	v_max_f32_e32 v2, 0, v2
	v_add_f32_e32 v17, v3, v40
	v_add_f32_e32 v3, v72, v46
	v_add_f32_e32 v21, v4, v41
	v_add_f32_e32 v4, v73, v47
	v_add_f32_e32 v18, v93, v32
	v_cvt_pk_f16_f32 v8, v8, v9
	v_cvt_pk_f16_f32 v9, v10, v11
	v_add_f32_e32 v3, 0, v3
	v_add_f32_e32 v4, 0, v4
	v_add_f32_e32 v22, v5, v42
	v_add_f32_e32 v5, v16, v48
	v_cvt_pk_f16_f32 v10, v7, v2
	v_add_u32_e32 v7, s33, v209
	v_add_f32_e32 v18, 0, v18
	v_max_f32_e32 v3, 0, v3
	v_max_f32_e32 v4, 0, v4
	v_add_f32_e32 v5, 0, v5
	v_or_b32_e32 v2, v1, v7
	v_max_f32_e32 v18, 0, v18
	v_max_f32_e32 v16, 0, v5
	v_cvt_pk_f16_f32 v11, v3, v4
	v_or_b32_e32 v4, 0x3c0, v2
	v_permlane32_swap_b32_e32 v18, v16
	v_ashrrev_i32_e32 v5, 31, v4
	v_ashrrev_i32_e32 v3, 31, v2
	v_add_f32_e32 v12, v88, v23
	v_add_f32_e32 v13, v89, v24
	v_add_f32_e32 v14, v90, v25
	v_add_f32_e32 v15, v91, v26
	v_permlane32_swap_b32_e32 v8, v10
	v_permlane32_swap_b32_e32 v9, v11
	v_lshl_add_u64 v[4:5], v[4:5], 4, s[16:17]
	v_cvt_pk_f16_f32 v1, v18, v16
	v_lshl_add_u64 v[2:3], v[2:3], 2, s[18:19]
	s_barrier
	v_add_f32_e32 v19, v92, v27
	global_store_dwordx4 v[4:5], v[8:11], off sc1
	global_store_dword v[2:3], v1, off offset:3840 sc1
	v_add_f32_e32 v1, 0, v12
	v_add_f32_e32 v2, 0, v13
	v_add_f32_e32 v3, 0, v14
	v_add_f32_e32 v4, 0, v15
	v_add_f32_e32 v1, v104, v1
	v_add_f32_e32 v2, v105, v2
	v_add_f32_e32 v3, v106, v3
	v_add_f32_e32 v4, v107, v4
	v_add_f32_e32 v5, 0, v19
	v_max_f32_e32 v1, 0, v1
	v_max_f32_e32 v2, 0, v2
	v_max_f32_e32 v3, 0, v3
	v_max_f32_e32 v4, 0, v4
	v_add_f32_e32 v5, v202, v5
	v_add_f32_e32 v6, v6, v43
	v_max_f32_e32 v8, 0, v5
	v_cvt_pk_f16_f32 v2, v1, v2
	v_cvt_pk_f16_f32 v3, v3, v4
	v_add_f32_e32 v1, 0, v20
	v_add_f32_e32 v4, 0, v17
	v_add_f32_e32 v5, 0, v21
	v_add_f32_e32 v9, 0, v22
	v_add_f32_e32 v1, v104, v1
	v_add_f32_e32 v4, v105, v4
	v_add_f32_e32 v5, v106, v5
	v_add_f32_e32 v9, v107, v9
	v_add_f32_e32 v6, 0, v6
	s_movk_i32 s0, 0x3e0
	v_max_f32_e32 v1, 0, v1
	v_max_f32_e32 v4, 0, v4
	v_max_f32_e32 v5, 0, v5
	v_max_f32_e32 v9, 0, v9
	v_add_f32_e32 v6, v202, v6
	v_or3_b32 v0, v0, v7, s0
	v_max_f32_e32 v10, 0, v6
	v_cvt_pk_f16_f32 v4, v1, v4
	v_cvt_pk_f16_f32 v5, v5, v9
	v_ashrrev_i32_e32 v1, 31, v0
	v_permlane32_swap_b32_e32 v2, v4
	v_permlane32_swap_b32_e32 v3, v5
	v_permlane32_swap_b32_e32 v8, v10
	v_lshl_add_u64 v[6:7], v[0:1], 4, s[16:17]
	global_store_dwordx4 v[6:7], v[2:5], off sc1
	v_lshl_add_u64 v[0:1], v[0:1], 2, s[18:19]
	s_nop 0
	v_cvt_pk_f16_f32 v2, v8, v10
	global_store_dword v[0:1], v2, off sc1
	s_endpgm

	.amdhsa_kernel _Z7k2_mfmaPK15HIP_vector_typeIjLj4EEPKjS2_PKfPS0_Pj
		.amdhsa_group_segment_fixed_size 0
		.amdhsa_private_segment_fixed_size 0
		.amdhsa_kernarg_size 304
		.amdhsa_user_sgpr_count 2
		.amdhsa_user_sgpr_dispatch_ptr 0
		.amdhsa_user_sgpr_queue_ptr 0
		.amdhsa_user_sgpr_kernarg_segment_ptr 1
		.amdhsa_user_sgpr_dispatch_id 0
		.amdhsa_user_sgpr_kernarg_preload_length 0
		.amdhsa_user_sgpr_kernarg_preload_offset 0
		.amdhsa_user_sgpr_private_segment_size 0
		.amdhsa_uses_dynamic_stack 0
		.amdhsa_enable_private_segment 0
		.amdhsa_system_sgpr_workgroup_id_x 1
		.amdhsa_system_sgpr_workgroup_id_y 0
		.amdhsa_system_sgpr_workgroup_id_z 0
		.amdhsa_system_sgpr_workgroup_info 0
		.amdhsa_system_vgpr_workitem_id 0
		.amdhsa_next_free_vgpr 245
		.amdhsa_next_free_sgpr 46
		.amdhsa_accum_offset 248
		.amdhsa_reserve_vcc 1
		.amdhsa_float_round_mode_32 0
		.amdhsa_float_round_mode_16_64 0
		.amdhsa_float_denorm_mode_32 3
		.amdhsa_float_denorm_mode_16_64 3
		.amdhsa_dx10_clamp 1
		.amdhsa_ieee_mode 1
		.amdhsa_fp16_overflow 0
		.amdhsa_tg_split 0
		.amdhsa_exception_fp_ieee_invalid_op 0
		.amdhsa_exception_fp_denorm_src 0
		.amdhsa_exception_fp_ieee_div_zero 0
		.amdhsa_exception_fp_ieee_overflow 0
		.amdhsa_exception_fp_ieee_underflow 0
		.amdhsa_exception_fp_ieee_inexact 0
		.amdhsa_exception_int_div_zero 0
	.end_amdhsa_kernel

.LBB6_511:
	s_or_b64 exec, exec, s[10:11]
	v_add_u32_e32 v6, s40, v194
	v_lshl_or_b32 v6, v6, 5, v202
	v_or3_b32 v6, v6, v190, s41
	s_lshl_b32 s40, s42, 20
	v_lshlrev_b32_e32 v213, 10, v6
	v_or_b32_e32 v6, s40, v206
	v_add_u32_e32 v192, v6, v213
	v_add_f32_e32 v71, 0, v71
	v_add_f32_e32 v80, 0, v72
	v_add_f32_e32 v81, 0, v73
	v_add_f32_e32 v189, 0, v74
	v_add_f32_e32 v203, 0, v75
	v_add_f32_e32 v87, 0, v87
	v_add_f32_e32 v204, 0, v88
	v_add_f32_e32 v205, 0, v89
	v_add_f32_e32 v220, 0, v90
	v_add_f32_e32 v221, 0, v91
	v_mfma_f32_32x32x16_f16 v[34:49], v[164:167], v[2:5], v[34:49]
	ds_read_b128 v[72:75], v209 offset:41184
	ds_read_b128 v[88:91], v211 offset:41184
	v_mfma_f32_32x32x16_f16 v[2:17], v[176:179], v[2:5], 0
	s_waitcnt lgkmcnt(3)
	v_mfma_f32_32x32x16_f16 v[34:49], v[160:163], v[184:187], v[34:49]
	v_mfma_f32_32x32x16_f16 v[2:17], v[172:175], v[184:187], v[2:17]
	v_mfma_f32_32x32x16_f16 v[34:49], v[168:171], v[180:183], v[34:49]
	v_mfma_f32_32x32x16_f16 v[2:17], v[164:167], v[180:183], v[2:17]
	ds_read_b128 v[180:183], v209 offset:44352
	ds_read_b128 v[184:187], v211 offset:44352
	s_waitcnt lgkmcnt(4)
	v_mfma_f32_32x32x16_f16 v[34:49], v[156:159], v[100:103], v[34:49]
	v_mfma_f32_32x32x16_f16 v[2:17], v[160:163], v[100:103], v[2:17]
	s_waitcnt lgkmcnt(3)
	v_mfma_f32_32x32x16_f16 v[2:17], v[168:171], v[72:75], v[2:17]
	v_add_f32_e32 v62, v205, v62
	v_add_f32_e32 v63, v220, v63
	v_add_f32_e32 v60, v87, v60
	v_add_f32_e32 v61, v204, v61
	v_max_f32_e32 v62, 0, v62
	v_max_f32_e32 v63, 0, v63
	v_max_f32_e32 v60, 0, v60
	s_waitcnt lgkmcnt(2)
	v_mfma_f32_32x32x16_f16 v[2:17], v[156:159], v[88:91], v[2:17]
	v_max_f32_e32 v61, 0, v61
	v_add_f32_e32 v28, v71, v28
	v_add_f32_e32 v29, v80, v29
	ds_read_b128 v[100:103], v209 offset:45408
	ds_read_b128 v[216:219], v211 offset:45408
	v_cvt_pk_f16_f32 v63, v62, v63
	v_cvt_pk_f16_f32 v62, v60, v61
	v_add_f32_e32 v60, v221, v64
	v_add_f32_e32 v30, v81, v30
	v_add_f32_e32 v31, v189, v31
	v_max_f32_e32 v28, 0, v28
	v_max_f32_e32 v29, 0, v29
	v_max_f32_e32 v64, 0, v60
	v_max_f32_e32 v30, 0, v30
	v_max_f32_e32 v31, 0, v31
	v_cvt_pk_f16_f32 v60, v28, v29
	v_add_f32_e32 v28, v203, v32
	v_cvt_pk_f16_f32 v61, v30, v31
	v_max_f32_e32 v30, 0, v28
	v_permlane32_swap_b32_e32 v60, v62
	v_permlane32_swap_b32_e32 v61, v63
	v_permlane32_swap_b32_e32 v30, v64
	v_lshl_add_u64 v[28:29], v[192:193], 4, s[16:17]
	global_store_dwordx4 v[28:29], v[60:63], off sc1
	v_cvt_pk_f16_f32 v30, v30, v64
	v_lshl_add_u64 v[28:29], v[192:193], 2, s[18:19]
	global_store_dword v[28:29], v30, off sc1
	s_waitcnt lgkmcnt(3)
	v_mfma_f32_32x32x16_f16 v[34:49], v[132:135], v[180:183], v[34:49]
	ds_read_b128 v[72:75], v209 offset:46464
	ds_read_b128 v[180:183], v211 offset:46464
	s_waitcnt lgkmcnt(4)
	v_mfma_f32_32x32x16_f16 v[34:49], v[140:143], v[184:187], v[34:49]
	s_waitcnt lgkmcnt(3)
	v_mfma_f32_32x32x16_f16 v[34:49], v[120:123], v[100:103], v[34:49]
	ds_read_b128 v[60:63], v209 offset:47520
	ds_read_b128 v[28:31], v211 offset:47520
	v_mfma_f32_32x32x16_f16 v[2:17], v[132:135], v[100:103], v[2:17]
	s_waitcnt lgkmcnt(4)
	v_mfma_f32_32x32x16_f16 v[34:49], v[152:155], v[216:219], v[34:49]
	v_mfma_f32_32x32x16_f16 v[2:17], v[140:143], v[216:219], v[2:17]
	s_waitcnt lgkmcnt(3)
	v_mfma_f32_32x32x16_f16 v[34:49], v[148:151], v[72:75], v[34:49]
	ds_read_b128 v[88:91], v209 offset:50688
	ds_read_b128 v[100:103], v211 offset:50688
	s_mov_b64 s[10:11], s[26:27]
	s_waitcnt vmcnt(3)
	ds_write_b128 v212, v[96:99] offset:16
	s_waitcnt vmcnt(2)
	ds_write_b32 v212, v188 offset:548
	v_mfma_f32_32x32x16_f16 v[2:17], v[120:123], v[72:75], v[2:17]
	s_waitcnt lgkmcnt(6)
	v_mfma_f32_32x32x16_f16 v[34:49], v[144:147], v[180:183], v[34:49]
	v_mfma_f32_32x32x16_f16 v[2:17], v[152:155], v[180:183], v[2:17]
	s_and_saveexec_b64 s[28:29], s[4:5]
	s_andn2_b64 s[10:11], s[26:27], exec
	s_and_b64 s[30:31], s[6:7], exec
	s_or_b64 s[10:11], s[10:11], s[30:31]
	ds_write_b32 v212, v188 offset:536
	s_or_b64 exec, exec, s[28:29]
	s_and_saveexec_b64 s[28:29], s[10:11]
	ds_write_b32 v212, v188 offset:560
	s_or_b64 exec, exec, s[28:29]
	s_waitcnt lgkmcnt(5)
	v_mfma_f32_32x32x16_f16 v[2:17], v[148:151], v[60:63], v[2:17]
	ds_read_b128 v[60:63], v209 offset:51744
	ds_read_b128 v[72:75], v211 offset:51744
	s_waitcnt lgkmcnt(6)
	v_mfma_f32_32x32x16_f16 v[2:17], v[144:147], v[28:31], v[2:17]
	s_waitcnt lgkmcnt(5)
	v_mfma_f32_32x32x16_f16 v[34:49], v[136:139], v[88:91], v[34:49]
	ds_read_b128 v[96:99], v209 offset:52800
	ds_read_b128 v[88:91], v211 offset:52800
	s_waitcnt lgkmcnt(6)
	v_mfma_f32_32x32x16_f16 v[34:49], v[108:111], v[100:103], v[34:49]
	s_and_saveexec_b64 s[10:11], s[0:1]
	s_cbranch_execz .LBB6_520
	s_mov_b64 s[30:31], s[26:27]
	ds_write_b128 v214, v[92:95] offset:16
	ds_write_b32 v214, v33 offset:548
	s_and_saveexec_b64 s[28:29], s[4:5]
	s_andn2_b64 s[30:31], s[26:27], exec
	s_and_b64 s[34:35], s[6:7], exec
	s_or_b64 s[30:31], s[30:31], s[34:35]
	ds_write_b32 v214, v33 offset:536
	s_or_b64 exec, exec, s[28:29]
	s_and_b64 exec, exec, s[30:31]
	ds_write_b32 v214, v33 offset:560

.LBB6_532:
	s_or_b64 exec, exec, s[34:35]
	v_mfma_f32_32x32x16_f16 v[56:71], v[164:167], v[72:75], v[56:71]
	ds_read_b128 v[218:221], v209 offset:3168
	ds_read_b128 v[222:225], v211 offset:3168
	v_mfma_f32_32x32x16_f16 v[72:87], v[176:179], v[72:75], 0
	s_waitcnt lgkmcnt(3)
	v_mfma_f32_32x32x16_f16 v[56:71], v[160:163], v[100:103], v[56:71]
	v_mfma_f32_32x32x16_f16 v[72:87], v[172:175], v[100:103], v[72:87]
	v_mfma_f32_32x32x16_f16 v[56:71], v[168:171], v[96:99], v[56:71]
	v_mfma_f32_32x32x16_f16 v[72:87], v[164:167], v[96:99], v[72:87]
	ds_read_b128 v[96:99], v209 offset:6336
	ds_read_b128 v[100:103], v211 offset:6336
	s_waitcnt lgkmcnt(4)
	v_mfma_f32_32x32x16_f16 v[56:71], v[156:159], v[92:95], v[56:71]
	v_mfma_f32_32x32x16_f16 v[72:87], v[160:163], v[92:95], v[72:87]
	v_add_f32_e32 v14, v187, v14
	v_add_f32_e32 v15, v188, v15
	s_waitcnt lgkmcnt(3)
	v_mfma_f32_32x32x16_f16 v[72:87], v[168:171], v[218:221], v[72:87]
	v_add_f32_e32 v12, v180, v12
	v_add_f32_e32 v13, v186, v13
	v_add_f32_e32 v14, 0, v14
	v_add_f32_e32 v15, 0, v15
	v_add_f32_e32 v12, 0, v12
	v_add_f32_e32 v13, 0, v13
	v_max_f32_e32 v14, 0, v14
	v_max_f32_e32 v15, 0, v15
	v_max_f32_e32 v12, 0, v12
	v_max_f32_e32 v13, 0, v13
	v_cvt_pk_f16_f32 v15, v14, v15
	v_cvt_pk_f16_f32 v14, v12, v13
	v_add_f32_e32 v12, v189, v16
	v_add_f32_e32 v12, 0, v12
	v_max_f32_e32 v16, 0, v12
	v_add_f32_e32 v12, v184, v46
	v_add_f32_e32 v13, v185, v47
	v_add_f32_e32 v12, 0, v12
	v_add_f32_e32 v13, 0, v13
	v_max_f32_e32 v12, 0, v12
	v_max_f32_e32 v13, 0, v13
	s_waitcnt lgkmcnt(2)
	v_mfma_f32_32x32x16_f16 v[72:87], v[156:159], v[222:225], v[72:87]
	v_cvt_pk_f16_f32 v13, v12, v13
	v_add_f32_e32 v12, v182, v44
	v_add_f32_e32 v44, v183, v45
	v_add_f32_e32 v12, 0, v12
	v_add_f32_e32 v44, 0, v44
	v_max_f32_e32 v12, 0, v12
	v_max_f32_e32 v44, 0, v44
	ds_read_b128 v[92:95], v209 offset:7392
	ds_read_b128 v[226:229], v211 offset:7392
	v_cvt_pk_f16_f32 v12, v12, v44
	v_add_f32_e32 v44, v181, v48
	v_add_f32_e32 v44, 0, v44
	v_max_f32_e32 v46, 0, v44
	v_permlane32_swap_b32_e32 v12, v14
	v_permlane32_swap_b32_e32 v13, v15
	v_permlane32_swap_b32_e32 v46, v16
	v_lshl_add_u64 v[44:45], s[20:21], 0, v[200:201]
	global_store_dwordx4 v[44:45], v[12:15], off sc1
	s_nop 1
	v_cvt_pk_f16_f32 v12, v46, v16
	global_store_dword v[198:199], v12, off sc1
	s_waitcnt lgkmcnt(3)
	v_mfma_f32_32x32x16_f16 v[56:71], v[132:135], v[96:99], v[56:71]
	ds_read_b128 v[96:99], v209 offset:8448
	ds_read_b128 v[180:183], v211 offset:8448
	s_waitcnt lgkmcnt(4)
	v_mfma_f32_32x32x16_f16 v[56:71], v[140:143], v[100:103], v[56:71]
	s_waitcnt lgkmcnt(3)
	v_mfma_f32_32x32x16_f16 v[56:71], v[120:123], v[92:95], v[56:71]
	ds_read_b128 v[12:15], v209 offset:9504
	ds_read_b128 v[44:47], v211 offset:9504
	v_mfma_f32_32x32x16_f16 v[72:87], v[132:135], v[92:95], v[72:87]
	s_waitcnt lgkmcnt(4)
	v_mfma_f32_32x32x16_f16 v[56:71], v[152:155], v[226:229], v[56:71]
	v_mfma_f32_32x32x16_f16 v[72:87], v[140:143], v[226:229], v[72:87]
	s_waitcnt lgkmcnt(3)
	v_mfma_f32_32x32x16_f16 v[56:71], v[148:151], v[96:99], v[56:71]
	s_mov_b64 s[34:35], s[26:27]
	v_mfma_f32_32x32x16_f16 v[72:87], v[120:123], v[96:99], v[72:87]
	ds_read_b128 v[100:103], v209 offset:12672
	ds_read_b128 v[96:99], v211 offset:12672
	s_waitcnt vmcnt(3)
	ds_write_b128 v212, v[88:91] offset:38032
	s_waitcnt vmcnt(2)
	ds_write_b32 v212, v49 offset:38564
	s_waitcnt lgkmcnt(6)
	v_mfma_f32_32x32x16_f16 v[56:71], v[144:147], v[180:183], v[56:71]
	v_mfma_f32_32x32x16_f16 v[72:87], v[152:155], v[180:183], v[72:87]
	s_and_saveexec_b64 s[36:37], s[4:5]
	s_andn2_b64 s[34:35], s[26:27], exec
	s_and_b64 s[38:39], s[6:7], exec
	s_or_b64 s[34:35], s[34:35], s[38:39]
	ds_write_b32 v212, v49 offset:38552
	s_or_b64 exec, exec, s[36:37]
	s_and_saveexec_b64 s[36:37], s[34:35]
	ds_write_b32 v212, v49 offset:38576
	s_or_b64 exec, exec, s[36:37]
	s_waitcnt lgkmcnt(5)
	v_mfma_f32_32x32x16_f16 v[72:87], v[148:151], v[12:15], v[72:87]
	ds_read_b128 v[92:95], v209 offset:13728
	ds_read_b128 v[12:15], v211 offset:13728
	s_waitcnt lgkmcnt(6)
	v_mfma_f32_32x32x16_f16 v[72:87], v[144:147], v[44:47], v[72:87]
	s_waitcnt lgkmcnt(5)
	v_mfma_f32_32x32x16_f16 v[56:71], v[136:139], v[100:103], v[56:71]
	ds_read_b128 v[88:91], v209 offset:14784
	ds_read_b128 v[44:47], v211 offset:14784
	s_waitcnt lgkmcnt(6)
	v_mfma_f32_32x32x16_f16 v[56:71], v[108:111], v[96:99], v[56:71]
	s_and_saveexec_b64 s[34:35], s[0:1]
	s_cbranch_execz .LBB6_541
	s_mov_b64 s[38:39], s[26:27]
	ds_write_b128 v214, v[28:31] offset:38032
	ds_write_b32 v214, v23 offset:38564
	s_and_saveexec_b64 s[36:37], s[4:5]
	s_andn2_b64 s[38:39], s[26:27], exec
	s_and_b64 s[42:43], s[6:7], exec
	s_or_b64 s[38:39], s[38:39], s[42:43]
	ds_write_b32 v214, v23 offset:38552
	s_or_b64 exec, exec, s[36:37]
	s_and_b64 exec, exec, s[38:39]
	ds_write_b32 v214, v23 offset:38576

.LBB6_552:
	s_or_b64 exec, exec, s[28:29]
	v_add_f32_e32 v39, v18, v39
	v_add_f32_e32 v202, v19, v40
	v_add_f32_e32 v203, v20, v41
	v_add_f32_e32 v204, v21, v42
	v_add_f32_e32 v205, v22, v43
	v_add_f32_e32 v7, v50, v7
	v_add_f32_e32 v218, v51, v8
	v_add_f32_e32 v219, v52, v9
	v_add_f32_e32 v220, v53, v10
	v_add_f32_e32 v221, v54, v11
	v_mfma_f32_32x32x16_f16 v[88:103], v[164:167], v[12:15], v[88:103]
	ds_read_b128 v[40:43], v209 offset:41184
	ds_read_b128 v[48:51], v211 offset:41184
	v_mfma_f32_32x32x16_f16 v[8:23], v[176:179], v[12:15], 0
	s_waitcnt lgkmcnt(3)
	v_mfma_f32_32x32x16_f16 v[88:103], v[160:163], v[188:191], v[88:103]
	v_mfma_f32_32x32x16_f16 v[8:23], v[172:175], v[188:191], v[8:23]
	v_mfma_f32_32x32x16_f16 v[88:103], v[168:171], v[184:187], v[88:103]
	v_mfma_f32_32x32x16_f16 v[8:23], v[164:167], v[184:187], v[8:23]
	ds_read_b128 v[52:55], v209 offset:44352
	ds_read_b128 v[184:187], v211 offset:44352
	s_waitcnt lgkmcnt(4)
	v_mfma_f32_32x32x16_f16 v[88:103], v[156:159], v[180:183], v[88:103]
	v_mfma_f32_32x32x16_f16 v[8:23], v[160:163], v[180:183], v[8:23]
	v_add_f32_e32 v84, v219, v84
	v_add_f32_e32 v85, v220, v85
	v_add_f32_e32 v84, 0, v84
	s_waitcnt lgkmcnt(3)
	v_mfma_f32_32x32x16_f16 v[8:23], v[168:171], v[40:43], v[8:23]
	v_add_f32_e32 v40, 0, v85
	v_max_f32_e32 v84, 0, v84
	v_max_f32_e32 v40, 0, v40
	v_cvt_pk_f16_f32 v43, v84, v40
	v_add_f32_e32 v7, v7, v82
	v_add_f32_e32 v40, v218, v83
	v_add_f32_e32 v7, 0, v7
	v_add_f32_e32 v40, 0, v40
	v_max_f32_e32 v7, 0, v7
	v_max_f32_e32 v40, 0, v40
	v_cvt_pk_f16_f32 v42, v7, v40
	v_add_f32_e32 v40, v203, v68
	v_add_f32_e32 v41, v204, v69
	v_add_f32_e32 v40, 0, v40
	v_add_f32_e32 v41, 0, v41
	v_max_f32_e32 v40, 0, v40
	v_max_f32_e32 v41, 0, v41
	s_waitcnt lgkmcnt(2)
	v_mfma_f32_32x32x16_f16 v[8:23], v[156:159], v[48:51], v[8:23]
	v_cvt_pk_f16_f32 v41, v40, v41
	v_add_f32_e32 v39, v39, v66
	v_add_f32_e32 v40, v202, v67
	v_add_f32_e32 v39, 0, v39
	v_add_f32_e32 v40, 0, v40
	v_max_f32_e32 v39, 0, v39
	v_max_f32_e32 v40, 0, v40
	ds_read_b128 v[180:183], v209 offset:45408
	ds_read_b128 v[188:191], v211 offset:45408
	v_add_f32_e32 v7, v221, v86
	v_cvt_pk_f16_f32 v40, v39, v40
	v_add_f32_e32 v39, v205, v70
	v_add_f32_e32 v7, 0, v7
	v_add_f32_e32 v39, 0, v39
	v_max_f32_e32 v7, 0, v7
	v_max_f32_e32 v39, 0, v39
	s_nop 1
	v_permlane32_swap_b32_e32 v39, v7
	v_permlane32_swap_b32_e32 v40, v42
	v_permlane32_swap_b32_e32 v41, v43
	v_lshl_add_u64 v[48:49], s[20:21], 0, v[194:195]
	v_cvt_pk_f16_f32 v7, v39, v7
	global_store_dwordx4 v[48:49], v[40:43], off offset:1024 sc1
	global_store_dword v[196:197], v7, off sc1
	s_waitcnt lgkmcnt(3)
	v_mfma_f32_32x32x16_f16 v[88:103], v[132:135], v[52:55], v[88:103]
	ds_read_b128 v[52:55], v209 offset:46464
	ds_read_b128 v[66:69], v211 offset:46464
	s_waitcnt lgkmcnt(4)
	v_mfma_f32_32x32x16_f16 v[88:103], v[140:143], v[184:187], v[88:103]
	s_waitcnt lgkmcnt(3)
	v_mfma_f32_32x32x16_f16 v[88:103], v[120:123], v[180:183], v[88:103]
	ds_read_b128 v[48:51], v209 offset:47520
	ds_read_b128 v[40:43], v211 offset:47520
	v_mfma_f32_32x32x16_f16 v[8:23], v[132:135], v[180:183], v[8:23]
	s_waitcnt lgkmcnt(4)
	v_mfma_f32_32x32x16_f16 v[88:103], v[152:155], v[188:191], v[88:103]
	v_mfma_f32_32x32x16_f16 v[8:23], v[140:143], v[188:191], v[8:23]
	s_waitcnt lgkmcnt(3)
	v_mfma_f32_32x32x16_f16 v[88:103], v[148:151], v[52:55], v[88:103]
	s_mov_b64 s[2:3], s[26:27]
	v_mfma_f32_32x32x16_f16 v[8:23], v[120:123], v[52:55], v[8:23]
	ds_read_b128 v[52:55], v209 offset:50688
	ds_read_b128 v[82:85], v211 offset:50688
	s_waitcnt vmcnt(3)
	ds_write_b128 v212, v[44:47] offset:16
	s_waitcnt vmcnt(2)
	ds_write_b32 v212, v87 offset:548
	s_waitcnt lgkmcnt(6)
	v_mfma_f32_32x32x16_f16 v[88:103], v[144:147], v[66:69], v[88:103]
	v_mfma_f32_32x32x16_f16 v[8:23], v[152:155], v[66:69], v[8:23]
	s_and_saveexec_b64 s[28:29], s[4:5]
	s_andn2_b64 s[2:3], s[26:27], exec
	s_and_b64 s[30:31], s[6:7], exec
	s_or_b64 s[2:3], s[2:3], s[30:31]
	ds_write_b32 v212, v87 offset:536
	s_or_b64 exec, exec, s[28:29]
	s_and_saveexec_b64 s[28:29], s[2:3]
	ds_write_b32 v212, v87 offset:560
	s_or_b64 exec, exec, s[28:29]
	s_waitcnt lgkmcnt(5)
	v_mfma_f32_32x32x16_f16 v[8:23], v[148:151], v[48:51], v[8:23]
	ds_read_b128 v[66:69], v209 offset:51744
	ds_read_b128 v[44:47], v211 offset:51744
	s_waitcnt lgkmcnt(6)
	v_mfma_f32_32x32x16_f16 v[8:23], v[144:147], v[40:43], v[8:23]
	s_waitcnt lgkmcnt(5)
	v_mfma_f32_32x32x16_f16 v[88:103], v[136:139], v[52:55], v[88:103]
	ds_read_b128 v[52:55], v209 offset:52800
	ds_read_b128 v[48:51], v211 offset:52800
	s_waitcnt lgkmcnt(6)
	v_mfma_f32_32x32x16_f16 v[88:103], v[108:111], v[82:85], v[88:103]
	s_and_saveexec_b64 s[2:3], s[0:1]
	s_cbranch_execz .LBB6_561
	s_mov_b64 s[30:31], s[26:27]
	ds_write_b128 v214, v[28:31] offset:16
	ds_write_b32 v214, v71 offset:548
	s_and_saveexec_b64 s[28:29], s[4:5]
	s_andn2_b64 s[30:31], s[26:27], exec
	s_and_b64 s[34:35], s[6:7], exec
	s_or_b64 s[30:31], s[30:31], s[34:35]
	ds_write_b32 v214, v71 offset:536
	s_or_b64 exec, exec, s[28:29]
	s_and_b64 exec, exec, s[30:31]
	ds_write_b32 v214, v71 offset:560

.LBB6_568:
	ds_read_b128 v[18:21], v209
	ds_read_b128 v[34:37], v209 offset:1056
	ds_read_b128 v[38:41], v211
	ds_read_b128 v[50:53], v209 offset:2112
	ds_read_b128 v[62:65], v211 offset:1056
	ds_read_b128 v[66:69], v211 offset:2112
	s_waitcnt lgkmcnt(5)
	v_mfma_f32_32x32x16_f16 v[18:33], v[176:179], v[18:21], 0
	s_waitcnt lgkmcnt(3)
	v_mfma_f32_32x32x16_f16 v[18:33], v[172:175], v[38:41], v[18:33]
	v_mfma_f32_32x32x16_f16 v[18:33], v[164:167], v[34:37], v[18:33]
	v_add_f32_e32 v54, v184, v100
	ds_read_b128 v[78:81], v209 offset:3168
	ds_read_b128 v[82:85], v211 offset:3168
	v_add_f32_e32 v54, 0, v54
	v_max_f32_e32 v55, 0, v54
	v_add_f32_e32 v54, v185, v101
	v_add_f32_e32 v1, v182, v98
	v_add_f32_e32 v17, v183, v99
	v_mfma_f32_32x32x16_f16 v[34:49], v[176:179], v[34:37], 0
	v_add_f32_e32 v54, 0, v54
	v_add_f32_e32 v1, 0, v1
	v_add_f32_e32 v70, v56, v93
	v_add_f32_e32 v17, 0, v17
	v_max_f32_e32 v56, 0, v54
	v_add_f32_e32 v54, v181, v102
	v_max_f32_e32 v1, 0, v1
	v_max_f32_e32 v17, 0, v17
	v_add_f32_e32 v54, 0, v54
	v_add_f32_e32 v71, v57, v94
	v_add_f32_e32 v77, v58, v95
	s_waitcnt lgkmcnt(3)
	v_mfma_f32_32x32x16_f16 v[18:33], v[160:163], v[62:65], v[18:33]
	v_add_f32_e32 v86, v59, v96
	v_max_f32_e32 v87, 0, v54
	v_add_f32_e32 v93, v60, v97
	v_cvt_pk_f16_f32 v54, v1, v17
	v_cvt_pk_f16_f32 v55, v55, v56
	v_mfma_f32_32x32x16_f16 v[34:49], v[172:175], v[62:65], v[34:49]
	v_mfma_f32_32x32x16_f16 v[18:33], v[168:171], v[50:53], v[18:33]
	v_mfma_f32_32x32x16_f16 v[34:49], v[164:167], v[50:53], v[34:49]
	ds_read_b128 v[50:53], v209 offset:6336
	ds_read_b128 v[58:61], v211 offset:6336
	s_waitcnt lgkmcnt(4)
	v_mfma_f32_32x32x16_f16 v[18:33], v[156:159], v[66:69], v[18:33]
	v_mfma_f32_32x32x16_f16 v[34:49], v[160:163], v[66:69], v[34:49]
	s_waitcnt lgkmcnt(3)
	v_mfma_f32_32x32x16_f16 v[34:49], v[168:171], v[78:81], v[34:49]
	v_add_f32_e32 v1, v180, v12
	v_add_f32_e32 v7, v72, v7
	v_add_f32_e32 v12, v186, v13
	v_add_f32_e32 v72, v73, v8
	v_add_f32_e32 v8, v187, v14
	v_add_f32_e32 v73, v74, v9
	v_add_f32_e32 v9, v188, v15
	ds_read_b128 v[62:65], v209 offset:7392
	ds_read_b128 v[66:69], v211 offset:7392
	v_add_f32_e32 v1, 0, v1
	v_add_f32_e32 v12, 0, v12
	v_add_f32_e32 v8, 0, v8
	v_add_f32_e32 v9, 0, v9
	v_add_f32_e32 v74, v75, v10
	v_add_f32_e32 v10, v189, v16
	v_max_f32_e32 v1, 0, v1
	v_max_f32_e32 v12, 0, v12
	v_max_f32_e32 v8, 0, v8
	v_max_f32_e32 v9, 0, v9
	v_add_f32_e32 v10, 0, v10
	v_max_f32_e32 v10, 0, v10
	v_cvt_pk_f16_f32 v56, v1, v12
	v_cvt_pk_f16_f32 v57, v8, v9
	v_add_u32_e32 v16, 0x3a0, v192
	v_mov_b32_e32 v17, 0
	v_permlane32_swap_b32_e32 v54, v56
	v_permlane32_swap_b32_e32 v55, v57
	v_permlane32_swap_b32_e32 v87, v10
	v_lshl_add_u64 v[8:9], v[16:17], 4, s[16:17]
	v_mov_b32_e32 v193, v17
	global_store_dwordx4 v[8:9], v[54:57], off sc1
	v_cvt_pk_f16_f32 v1, v87, v10
	v_lshl_add_u64 v[8:9], v[192:193], 2, s[18:19]
	s_waitcnt lgkmcnt(4)
	v_mfma_f32_32x32x16_f16 v[34:49], v[156:159], v[82:85], v[34:49]
	v_add_f32_e32 v75, v76, v11
	global_store_dword v[8:9], v1, off offset:3712 sc1
	s_waitcnt lgkmcnt(3)
	v_mfma_f32_32x32x16_f16 v[18:33], v[132:135], v[50:53], v[18:33]
	ds_read_b128 v[8:11], v209 offset:8448
	ds_read_b128 v[12:15], v211 offset:8448
	s_waitcnt lgkmcnt(4)
	v_mfma_f32_32x32x16_f16 v[18:33], v[140:143], v[58:61], v[18:33]
	s_waitcnt lgkmcnt(3)
	v_mfma_f32_32x32x16_f16 v[18:33], v[120:123], v[62:65], v[18:33]
	ds_read_b128 v[50:53], v209 offset:9504
	ds_read_b128 v[54:57], v211 offset:9504
	v_mfma_f32_32x32x16_f16 v[34:49], v[132:135], v[62:65], v[34:49]
	s_waitcnt lgkmcnt(4)
	v_mfma_f32_32x32x16_f16 v[18:33], v[152:155], v[66:69], v[18:33]
	v_mfma_f32_32x32x16_f16 v[34:49], v[140:143], v[66:69], v[34:49]
	s_waitcnt lgkmcnt(3)
	v_mfma_f32_32x32x16_f16 v[18:33], v[148:151], v[8:11], v[18:33]
	v_mfma_f32_32x32x16_f16 v[34:49], v[120:123], v[8:11], v[34:49]
	ds_read_b128 v[8:11], v209 offset:12672
	ds_read_b128 v[58:61], v211 offset:12672
	s_waitcnt lgkmcnt(4)
	v_mfma_f32_32x32x16_f16 v[18:33], v[144:147], v[12:15], v[18:33]
	v_mfma_f32_32x32x16_f16 v[34:49], v[152:155], v[12:15], v[34:49]
	s_waitcnt lgkmcnt(3)
	v_mfma_f32_32x32x16_f16 v[34:49], v[148:151], v[50:53], v[34:49]
	ds_read_b128 v[12:15], v209 offset:13728
	ds_read_b128 v[50:53], v211 offset:13728
	s_waitcnt lgkmcnt(4)
	v_mfma_f32_32x32x16_f16 v[34:49], v[144:147], v[54:57], v[34:49]
	s_waitcnt lgkmcnt(3)
	v_mfma_f32_32x32x16_f16 v[18:33], v[136:139], v[8:11], v[18:33]
	ds_read_b128 v[8:11], v209 offset:14784
	ds_read_b128 v[54:57], v211 offset:14784
	s_waitcnt lgkmcnt(4)
	v_mfma_f32_32x32x16_f16 v[18:33], v[108:111], v[58:61], v[18:33]
	s_waitcnt lgkmcnt(3)
	v_mfma_f32_32x32x16_f16 v[18:33], v[128:131], v[12:15], v[18:33]
	v_mfma_f32_32x32x16_f16 v[34:49], v[136:139], v[12:15], v[34:49]
	ds_read_b128 v[12:15], v209 offset:15840
	ds_read_b128 v[58:61], v211 offset:15840
	s_waitcnt lgkmcnt(4)
	v_mfma_f32_32x32x16_f16 v[18:33], v[124:127], v[50:53], v[18:33]
	v_mfma_f32_32x32x16_f16 v[34:49], v[108:111], v[50:53], v[34:49]
	s_waitcnt lgkmcnt(3)
	v_mfma_f32_32x32x16_f16 v[18:33], v[116:119], v[8:11], v[18:33]
	v_mfma_f32_32x32x16_f16 v[34:49], v[128:131], v[8:11], v[34:49]
	s_waitcnt lgkmcnt(2)
	v_mfma_f32_32x32x16_f16 v[18:33], v[112:115], v[54:57], v[18:33]
	v_mfma_f32_32x32x16_f16 v[34:49], v[124:127], v[54:57], v[34:49]
	s_waitcnt lgkmcnt(1)
	v_mfma_f32_32x32x16_f16 v[34:49], v[116:119], v[12:15], v[34:49]
	s_waitcnt lgkmcnt(0)
	v_mfma_f32_32x32x16_f16 v[34:49], v[112:115], v[58:61], v[34:49]
	s_nop 6
	v_add_f32_e32 v1, v70, v28
	v_add_f32_e32 v8, v71, v29
	v_add_f32_e32 v1, 0, v1
	v_add_f32_e32 v8, 0, v8
	v_max_f32_e32 v1, 0, v1
	v_max_f32_e32 v8, 0, v8
	v_add_f32_e32 v9, v77, v30
	v_add_f32_e32 v10, v86, v31
	v_cvt_pk_f16_f32 v8, v1, v8
	v_add_f32_e32 v1, v7, v44
	v_add_f32_e32 v7, v2, v39
	v_add_f32_e32 v2, v72, v45
	v_add_f32_e32 v9, 0, v9
	v_add_f32_e32 v10, 0, v10
	v_add_f32_e32 v1, 0, v1
	v_add_f32_e32 v2, 0, v2
	v_max_f32_e32 v9, 0, v9
	v_max_f32_e32 v10, 0, v10
	v_max_f32_e32 v1, 0, v1
	v_max_f32_e32 v2, 0, v2
	v_add_f32_e32 v20, v3, v40
	v_add_f32_e32 v3, v73, v46
	v_add_f32_e32 v21, v4, v41
	v_add_f32_e32 v4, v74, v47
	v_add_f32_e32 v11, v93, v32
	v_cvt_pk_f16_f32 v9, v9, v10
	v_add_f32_e32 v3, 0, v3
	v_add_f32_e32 v4, 0, v4
	v_add_f32_e32 v22, v5, v42
	v_add_f32_e32 v5, v75, v48
	v_cvt_pk_f16_f32 v10, v1, v2
	v_add_u32_e32 v1, s40, v213
	v_add_f32_e32 v11, 0, v11
	v_max_f32_e32 v3, 0, v3
	v_max_f32_e32 v4, 0, v4
	v_add_f32_e32 v5, 0, v5
	v_or_b32_e32 v2, v206, v1
	v_add_f32_e32 v12, v88, v23
	v_max_f32_e32 v18, 0, v11
	v_max_f32_e32 v23, 0, v5
	v_cvt_pk_f16_f32 v11, v3, v4
	v_or_b32_e32 v16, 0x3c0, v2
	v_permlane32_swap_b32_e32 v8, v10
	v_permlane32_swap_b32_e32 v9, v11
	v_permlane32_swap_b32_e32 v18, v23
	v_lshl_add_u64 v[4:5], v[16:17], 4, s[16:17]
	v_mov_b32_e32 v3, v17
	s_barrier
	v_add_f32_e32 v13, v89, v24
	v_add_f32_e32 v14, v90, v25
	v_add_f32_e32 v15, v91, v26
	global_store_dwordx4 v[4:5], v[8:11], off sc1
	v_cvt_pk_f16_f32 v4, v18, v23
	v_lshl_add_u64 v[2:3], v[2:3], 2, s[18:19]
	global_store_dword v[2:3], v4, off offset:3840 sc1
	v_add_f32_e32 v2, 0, v12
	v_add_f32_e32 v3, 0, v13
	v_add_f32_e32 v4, 0, v14
	v_add_f32_e32 v5, 0, v15
	v_add_f32_e32 v2, v104, v2
	v_add_f32_e32 v3, v105, v3
	v_add_f32_e32 v4, v106, v4
	v_add_f32_e32 v5, v107, v5
	v_max_f32_e32 v2, 0, v2
	v_max_f32_e32 v3, 0, v3
	v_max_f32_e32 v4, 0, v4
	v_max_f32_e32 v5, 0, v5
	v_add_f32_e32 v19, v92, v27
	v_add_f32_e32 v6, v6, v43
	v_cvt_pk_f16_f32 v2, v2, v3
	v_cvt_pk_f16_f32 v3, v4, v5
	v_add_f32_e32 v4, 0, v7
	v_add_f32_e32 v5, 0, v20
	v_add_f32_e32 v7, 0, v21
	v_add_f32_e32 v9, 0, v22
	v_add_f32_e32 v8, 0, v19
	v_add_f32_e32 v4, v104, v4
	v_add_f32_e32 v5, v105, v5
	v_add_f32_e32 v7, v106, v7
	v_add_f32_e32 v9, v107, v9
	v_add_f32_e32 v6, 0, v6
	v_add_f32_e32 v8, v207, v8
	v_max_f32_e32 v4, 0, v4
	v_max_f32_e32 v5, 0, v5
	v_max_f32_e32 v7, 0, v7
	v_max_f32_e32 v9, 0, v9
	v_add_f32_e32 v6, v207, v6
	s_movk_i32 s0, 0x3e0
	v_max_f32_e32 v8, 0, v8
	v_max_f32_e32 v6, 0, v6
	v_cvt_pk_f16_f32 v4, v4, v5
	v_cvt_pk_f16_f32 v5, v7, v9
	v_or3_b32 v16, v0, v1, s0
	v_permlane32_swap_b32_e32 v2, v4
	v_permlane32_swap_b32_e32 v3, v5
	v_permlane32_swap_b32_e32 v8, v6
	v_lshl_add_u64 v[0:1], v[16:17], 4, s[16:17]
	global_store_dwordx4 v[0:1], v[2:5], off sc1
	v_lshl_add_u64 v[0:1], v[16:17], 2, s[18:19]
	s_nop 0
	v_cvt_pk_f16_f32 v2, v8, v6
	global_store_dword v[0:1], v2, off sc1
	s_endpgm

	.text
	.protected	_Z8k3t_mfmaILi1EEvPK15HIP_vector_typeIjLj4EEPKjS3_PKfPf
	.globl	_Z8k3t_mfmaILi1EEvPK15HIP_vector_typeIjLj4EEPKjS3_PKfPf
	.p2align	8
	.type	_Z8k3t_mfmaILi1EEvPK15HIP_vector_typeIjLj4EEPKjS3_PKfPf,@function

.LBB8_145:
	s_or_b64 exec, exec, s[14:15]
	v_add_f32_e32 v224, v45, v9
	v_mov_b32_e32 v45, v43
	v_mov_b32_e32 v9, v7
	v_pk_add_f32 v[166:167], v[44:45], v[8:9]
	v_add_u32_e32 v6, s33, v191
	v_add_lshl_u32 v6, v6, v208, 5
	s_add_i32 s14, s50, s56
	v_add3_u32 v6, s14, v6, v207
	s_lshl_b32 s15, s52, 15
	v_lshl_or_b32 v6, v6, 10, v190
	s_lshl_b32 s14, s53, 20
	s_and_b32 s15, s15, 0xe0000
	v_ashrrev_i32_e32 v7, 31, v6
	s_or_b32 s14, s14, s15
	s_lshl_b32 s15, s51, 12
	v_lshl_add_u64 v[174:175], v[6:7], 2, s[24:25]
	v_lshl_add_u32 v6, v182, 15, s14
	s_and_b32 s15, s15, 0x6000
	v_or_b32_e32 v6, s15, v6
	v_add_u32_e32 v7, v177, v176
	v_lshl_add_u32 v217, v7, 10, v6
	v_or_b32_e32 v6, v217, v190
	v_add_u32_e32 v6, 0xffff7c00, v6
	v_ashrrev_i32_e32 v7, 31, v6
	v_lshl_add_u64 v[176:177], v[6:7], 2, s[18:19]
	v_lshl_add_u32 v6, v179, 15, s14
	v_or_b32_e32 v6, s15, v6
	v_add_u32_e32 v7, v178, v193
	v_lshl_add_u32 v218, v7, 10, v6
	v_or_b32_e32 v6, v218, v190
	v_add_u32_e32 v6, 0xfffffc00, v6
	v_ashrrev_i32_e32 v7, 31, v6
	v_lshl_add_u64 v[178:179], v[6:7], 2, s[18:19]
	v_lshl_add_u32 v6, v181, 15, s14
	v_or_b32_e32 v6, s15, v6
	v_add_u32_e32 v7, v183, v180
	v_lshl_add_u32 v219, v7, 10, v6
	v_or_b32_e32 v6, v219, v190
	v_add_u32_e32 v6, 0xffff7c00, v6
	v_ashrrev_i32_e32 v7, 31, v6
	v_lshl_add_u64 v[180:181], v[6:7], 2, s[18:19]
	v_lshl_or_b32 v6, v195, 15, s14
	v_or_b32_e32 v6, s15, v6
	v_add_u32_e32 v7, v194, v193
	v_lshl_add_u32 v220, v7, 10, v6
	v_or_b32_e32 v6, v220, v190
	v_add_u32_e32 v6, 0xffff7c00, v6
	v_ashrrev_i32_e32 v7, 31, v6
	s_mov_b32 s57, 2
	v_lshl_add_u64 v[182:183], v[6:7], 2, s[18:19]
	v_mov_b32_e32 v213, 0
	s_mov_b64 s[36:37], 0
	s_mov_b32 s58, 0xffff7e80
	s_movk_i32 s59, 0xfe80
	s_mov_b32 s60, 0xffff7ea0
	s_movk_i32 s61, 0xfea0
	v_mov_b32_e32 v216, 0
	v_mov_b32_e32 v215, 0
	v_mov_b32_e32 v214, 0
	s_waitcnt lgkmcnt(0)
	v_mbcnt_lo_u32_b32 v250, -1, 0
	v_mbcnt_hi_u32_b32 v250, -1, v250
	v_and_b32_e32 v250, 31, v250
	v_mul_u32_u24_e32 v251, 11, v250
	v_lshrrev_b32_e32 v251, 5, v251
	v_mul_u32_u24_e32 v251, 3, v251
	v_sub_u32_e32 v250, v250, v251
	v_mul_u32_u24_e32 v252, 12, v250
	v_add_u32_e32 v251, 2, v250
	v_mul_u32_u24_e32 v253, 11, v251
	v_lshrrev_b32_e32 v253, 5, v253
	v_mul_u32_u24_e32 v253, 3, v253
	v_sub_u32_e32 v251, v251, v253
	v_mul_u32_u24_e32 v251, 12, v251
	v_add_u32_e32 v251, -12, v251
	v_add_u32_e32 v250, 1, v250
	v_mul_u32_u24_e32 v253, 11, v250
	v_lshrrev_b32_e32 v253, 5, v253
	v_mul_u32_u24_e32 v253, 3, v253
	v_sub_u32_e32 v250, v250, v253
	v_mul_u32_u24_e32 v250, 12, v250
	v_add_u32_e32 v250, 0xffffffe8, v250
	v_add_u32_e32 v238, v202, v251
	v_add_u32_e32 v239, v202, v252
	v_add_u32_e32 v240, v202, v250
	v_add_u32_e32 v241, v203, v251
	v_add_u32_e32 v242, v203, v252
	v_add_u32_e32 v243, v203, v250
	v_add_u32_e32 v244, v209, v251
	v_add_u32_e32 v245, v209, v252
	v_add_u32_e32 v246, v209, v250
	v_add_u32_e32 v247, v210, v251
	v_add_u32_e32 v248, v210, v252
	v_add_u32_e32 v249, v210, v250
	s_barrier

.LBB8_158:
	s_or_b64 exec, exec, s[44:45]
	s_waitcnt lgkmcnt(3)
	v_mfma_f32_32x32x16_f16 v[26:41], v[94:97], v[50:53], v[26:41]
	ds_read_b128 v[54:57], v204 offset:13728
	ds_read_b128 v[50:53], v205 offset:13728
	s_mov_b64 s[44:45], s[34:35]
	s_waitcnt vmcnt(1)
	ds_write_b128 v202, v[46:49] offset:63376
	s_waitcnt vmcnt(0)
	ds_write_b32 v238, v226 offset:63908
	s_waitcnt lgkmcnt(6)
	v_mfma_f32_32x32x16_f16 v[26:41], v[86:89], v[162:165], v[26:41]
	s_and_saveexec_b64 s[46:47], s[6:7]
	s_andn2_b64 s[44:45], s[34:35], exec
	s_and_b64 s[48:49], s[8:9], exec
	s_or_b64 s[44:45], s[44:45], s[48:49]
	ds_write_b32 v239, v226 offset:63896
	s_or_b64 exec, exec, s[46:47]
	s_and_saveexec_b64 s[46:47], s[44:45]
	ds_write_b32 v240, v226 offset:63920
	s_or_b64 exec, exec, s[46:47]
	s_waitcnt lgkmcnt(5)
	v_mfma_f32_32x32x16_f16 v[26:41], v[90:93], v[154:157], v[26:41]
	ds_read_b128 v[154:157], v204 offset:14784
	ds_read_b128 v[46:49], v205 offset:14784
	v_add_f32_e32 v221, v171, v22
	v_add_f32_e32 v222, v167, v23
	s_waitcnt lgkmcnt(6)
	v_mfma_f32_32x32x16_f16 v[26:41], v[82:85], v[158:161], v[26:41]
	s_and_saveexec_b64 s[44:45], s[12:13]
	s_xor_b64 s[44:45], exec, s[44:45]
	v_add_f32_e32 v222, v167, v23
	ds_write2st64_b32 v206, v221, v222 offset0:4 offset1:5
	s_andn2_saveexec_b64 s[44:45], s[44:45]
	s_or_b64 exec, exec, s[44:45]
	v_add_f32_e32 v226, v166, v24
	v_add_f32_e32 v223, v224, v25
	s_and_saveexec_b64 s[44:45], s[12:13]
	s_xor_b64 s[44:45], exec, s[44:45]
	v_add_f32_e32 v223, v224, v25
	ds_write2st64_b32 v206, v226, v223 offset0:6 offset1:7
	s_andn2_saveexec_b64 s[44:45], s[44:45]
	s_or_b64 exec, exec, s[44:45]
	s_waitcnt lgkmcnt(5)
	v_mfma_f32_32x32x16_f16 v[26:41], v[78:81], v[54:57], v[26:41]
	ds_read_b128 v[54:57], v204 offset:15840
	ds_read_b128 v[22:25], v205 offset:15840
	s_mov_b64 s[44:45], s[34:35]
	ds_write_b128 v203, v[42:45] offset:63376
	ds_write_b32 v241, v228 offset:63908
	s_waitcnt lgkmcnt(8)
	v_mfma_f32_32x32x16_f16 v[26:41], v[58:61], v[50:53], v[26:41]
	s_and_saveexec_b64 s[46:47], s[6:7]
	s_andn2_b64 s[44:45], s[34:35], exec
	s_and_b64 s[48:49], s[8:9], exec
	s_or_b64 s[44:45], s[44:45], s[48:49]
	ds_write_b32 v242, v228 offset:63896
	s_or_b64 exec, exec, s[46:47]
	s_and_saveexec_b64 s[46:47], s[44:45]
	ds_write_b32 v243, v228 offset:63920
	s_or_b64 exec, exec, s[46:47]
	s_waitcnt lgkmcnt(5)
	v_mfma_f32_32x32x16_f16 v[26:41], v[70:73], v[154:157], v[26:41]
	s_waitcnt lgkmcnt(4)
	v_mfma_f32_32x32x16_f16 v[26:41], v[62:65], v[46:49], v[26:41]
	s_and_saveexec_b64 s[44:45], s[2:3]
	s_cbranch_execz .LBB8_175
	s_mov_b64 s[48:49], s[34:35]
	ds_write_b128 v209, v[10:13] offset:63376
	ds_write_b32 v244, v225 offset:63908
	s_and_saveexec_b64 s[46:47], s[6:7]
	s_andn2_b64 s[48:49], s[34:35], exec
	s_and_b64 s[62:63], s[8:9], exec
	s_or_b64 s[48:49], s[48:49], s[62:63]
	ds_write_b32 v245, v225 offset:63896
	s_or_b64 exec, exec, s[46:47]
	s_and_b64 exec, exec, s[48:49]
	ds_write_b32 v246, v225 offset:63920
.LBB8_175:
	s_or_b64 exec, exec, s[44:45]
	s_waitcnt lgkmcnt(3)
	v_mfma_f32_32x32x16_f16 v[26:41], v[74:77], v[54:57], v[26:41]
	s_waitcnt lgkmcnt(2)
	v_mfma_f32_32x32x16_f16 v[26:41], v[66:69], v[22:25], v[26:41]
	s_and_saveexec_b64 s[44:45], s[4:5]
	s_cbranch_execz .LBB8_180
	s_mov_b64 s[48:49], s[34:35]
	ds_write_b128 v210, v[6:9] offset:63376
	ds_write_b32 v247, v227 offset:63908
	s_and_saveexec_b64 s[46:47], s[6:7]
	s_andn2_b64 s[48:49], s[34:35], exec
	s_and_b64 s[62:63], s[8:9], exec
	s_or_b64 s[48:49], s[48:49], s[62:63]
	ds_write_b32 v248, v227 offset:63896
	s_or_b64 exec, exec, s[46:47]
	s_and_b64 exec, exec, s[48:49]
	ds_write_b32 v249, v227 offset:63920

.LBB8_192:
	s_or_b64 exec, exec, s[14:15]
	s_waitcnt lgkmcnt(3)
	v_mfma_f32_32x32x16_f16 v[38:53], v[94:97], v[154:157], v[38:53]
	ds_read_b128 v[158:161], v211 offset:13728
	ds_read_b128 v[154:157], v212 offset:13728
	s_mov_b64 s[14:15], s[34:35]
	s_waitcnt vmcnt(1)
	ds_write_b128 v202, v[54:57] offset:16
	s_waitcnt vmcnt(0)
	ds_write_b32 v238, v228 offset:548
	s_waitcnt lgkmcnt(6)
	v_mfma_f32_32x32x16_f16 v[38:53], v[86:89], v[170:173], v[38:53]
	s_and_saveexec_b64 s[38:39], s[6:7]
	s_andn2_b64 s[14:15], s[34:35], exec
	s_and_b64 s[40:41], s[8:9], exec
	s_or_b64 s[14:15], s[14:15], s[40:41]
	ds_write_b32 v239, v228 offset:536
	s_or_b64 exec, exec, s[38:39]
	s_and_saveexec_b64 s[38:39], s[14:15]
	ds_write_b32 v240, v228 offset:560
	s_or_b64 exec, exec, s[38:39]
	v_add_f32_e32 v19, v3, v19
	v_add_f32_e32 v2, v2, v18
	s_waitcnt lgkmcnt(5)
	v_mfma_f32_32x32x16_f16 v[38:53], v[90:93], v[162:165], v[38:53]
	ds_read_b128 v[162:165], v211 offset:14784
	ds_read_b128 v[54:57], v212 offset:14784
	v_mov_b32_e32 v170, v34
	v_mov_b32_e32 v171, v14
	v_mov_b32_e32 v3, v30
	v_pk_add_f32 v[170:171], v[170:171], v[2:3]
	v_add_f32_e32 v221, v19, v35
	v_mov_b32_e32 v3, v27
	s_waitcnt lgkmcnt(6)
	v_mfma_f32_32x32x16_f16 v[38:53], v[82:85], v[166:169], v[38:53]
	s_and_saveexec_b64 s[14:15], s[12:13]
	s_xor_b64 s[14:15], exec, s[14:15]
	v_add_f32_e32 v221, v19, v35
	v_mov_b32_e32 v3, v27
	ds_write2st64_b32 v206, v170, v221 offset1:1
	s_andn2_saveexec_b64 s[14:15], s[14:15]
	s_or_b64 exec, exec, s[14:15]
	v_add_f32_e32 v2, v5, v21
	v_add_f32_e32 v4, v4, v20
	v_add_f32_e32 v223, v4, v36
	v_add_f32_e32 v222, v2, v37
	v_mov_b32_e32 v5, v29
	s_and_saveexec_b64 s[14:15], s[12:13]
	s_xor_b64 s[14:15], exec, s[14:15]
	v_add_f32_e32 v222, v2, v37
	v_mov_b32_e32 v5, v29
	ds_write2st64_b32 v206, v223, v222 offset0:2 offset1:3
	s_andn2_saveexec_b64 s[14:15], s[14:15]
	s_or_b64 exec, exec, s[14:15]
	s_waitcnt lgkmcnt(5)
	v_mfma_f32_32x32x16_f16 v[38:53], v[78:81], v[158:161], v[38:53]
	ds_read_b128 v[34:37], v211 offset:15840
	ds_read_b128 v[18:21], v212 offset:15840
	s_mov_b64 s[14:15], s[34:35]
	ds_write_b128 v203, v[22:25] offset:16
	ds_write_b32 v241, v225 offset:548
	s_waitcnt lgkmcnt(8)
	v_mfma_f32_32x32x16_f16 v[38:53], v[58:61], v[154:157], v[38:53]
	s_and_saveexec_b64 s[38:39], s[6:7]
	s_andn2_b64 s[14:15], s[34:35], exec
	s_and_b64 s[40:41], s[8:9], exec
	s_or_b64 s[14:15], s[14:15], s[40:41]
	ds_write_b32 v242, v225 offset:536
	s_or_b64 exec, exec, s[38:39]
	s_and_saveexec_b64 s[38:39], s[14:15]
	ds_write_b32 v243, v225 offset:560
	s_or_b64 exec, exec, s[38:39]
	s_waitcnt lgkmcnt(5)
	v_mfma_f32_32x32x16_f16 v[38:53], v[70:73], v[162:165], v[38:53]
	s_waitcnt lgkmcnt(4)
	v_mfma_f32_32x32x16_f16 v[38:53], v[62:65], v[54:57], v[38:53]
	s_and_saveexec_b64 s[14:15], s[2:3]
	s_cbranch_execz .LBB8_209
	s_mov_b64 s[40:41], s[34:35]
	ds_write_b128 v209, v[10:13] offset:16
	ds_write_b32 v244, v227 offset:548
	s_and_saveexec_b64 s[38:39], s[6:7]
	s_andn2_b64 s[40:41], s[34:35], exec
	s_and_b64 s[42:43], s[8:9], exec
	s_or_b64 s[40:41], s[40:41], s[42:43]
	ds_write_b32 v245, v227 offset:536
	s_or_b64 exec, exec, s[38:39]
	s_and_b64 exec, exec, s[40:41]
	ds_write_b32 v246, v227 offset:560
.LBB8_209:
	s_or_b64 exec, exec, s[14:15]
	s_waitcnt lgkmcnt(3)
	v_mfma_f32_32x32x16_f16 v[38:53], v[74:77], v[34:37], v[38:53]
	s_waitcnt lgkmcnt(2)
	v_mfma_f32_32x32x16_f16 v[38:53], v[66:69], v[18:21], v[38:53]
	s_and_saveexec_b64 s[14:15], s[4:5]
	s_cbranch_execz .LBB8_214
	s_mov_b64 s[40:41], s[34:35]
	ds_write_b128 v210, v[6:9] offset:16
	ds_write_b32 v247, v224 offset:548
	s_and_saveexec_b64 s[38:39], s[6:7]
	s_andn2_b64 s[40:41], s[34:35], exec
	s_and_b64 s[42:43], s[8:9], exec
	s_or_b64 s[40:41], s[40:41], s[42:43]
	ds_write_b32 v248, v224 offset:536
	s_or_b64 exec, exec, s[38:39]
	s_and_b64 exec, exec, s[40:41]
	ds_write_b32 v249, v224 offset:560

.LBB8_357:
	s_or_b64 exec, exec, s[14:15]
	v_add_f32_e32 v179, v31, v7
	v_mov_b32_e32 v31, v29
	v_mov_b32_e32 v7, v5
	v_pk_add_f32 v[166:167], v[30:31], v[6:7]
	s_xor_b64 s[22:23], s[2:3], -1
	s_xor_b64 s[26:27], s[4:5], -1
	v_add3_u32 v4, v191, s33, v185
	s_add_i32 s14, s50, s47
	v_lshl_add_u32 v4, v4, 5, s14
	s_lshl_b32 s15, s53, 20
	s_lshl_b32 s34, s51, 12
	v_add_lshl_u32 v199, v4, v186, 10
	v_lshl_or_b32 v4, v195, 15, s15
	s_and_b32 s34, s34, 0x6000
	v_or_b32_e32 v4, s34, v4
	v_add_u32_e32 v5, v194, v193
	v_lshl_add_u32 v194, v5, 10, v4
	v_lshl_add_u32 v4, v165, 15, s15
	v_or_b32_e32 v4, s34, v4
	v_add_u32_e32 v5, v175, v164
	v_lshl_add_u32 v201, v5, 10, v4
	v_lshl_or_b32 v4, v171, 15, s15
	v_or_b32_e32 v4, s34, v4
	v_add_u32_e32 v5, v170, v193
	s_lshl_b32 s14, s52, 15
	v_lshl_add_u32 v193, v5, 10, v4
	v_lshl_add_u32 v4, v174, 15, s15
	s_and_b32 s14, s14, 0xe0000
	v_or_b32_e32 v4, s34, v4
	v_add_u32_e32 v5, v173, v172
	v_or_b32_e32 v195, s14, v190
	v_lshl_add_u32 v202, v5, 10, v4
	v_mov_b32_e32 v203, 0
	s_mov_b32 s48, 2
	s_mov_b32 s49, 0xffff7c80
	s_movk_i32 s51, 0xfc80
	s_mov_b32 s52, 0xffff7ca0
	s_movk_i32 s53, 0xfca0
	v_mov_b32_e32 v204, 0
	v_mov_b32_e32 v205, 0
	v_mov_b32_e32 v206, 0
	s_waitcnt lgkmcnt(0)
	v_mbcnt_lo_u32_b32 v250, -1, 0
	v_mbcnt_hi_u32_b32 v250, -1, v250
	v_and_b32_e32 v250, 31, v250
	v_mul_u32_u24_e32 v251, 11, v250
	v_lshrrev_b32_e32 v251, 5, v251
	v_mul_u32_u24_e32 v251, 3, v251
	v_sub_u32_e32 v250, v250, v251
	v_mul_u32_u24_e32 v252, 12, v250
	v_add_u32_e32 v251, 2, v250
	v_mul_u32_u24_e32 v253, 11, v251
	v_lshrrev_b32_e32 v253, 5, v253
	v_mul_u32_u24_e32 v253, 3, v253
	v_sub_u32_e32 v251, v251, v253
	v_mul_u32_u24_e32 v251, 12, v251
	v_add_u32_e32 v251, -12, v251
	v_add_u32_e32 v250, 1, v250
	v_mul_u32_u24_e32 v253, 11, v250
	v_lshrrev_b32_e32 v253, 5, v253
	v_mul_u32_u24_e32 v253, 3, v253
	v_sub_u32_e32 v250, v250, v253
	v_mul_u32_u24_e32 v250, 12, v250
	v_add_u32_e32 v250, 0xffffffe8, v250
	v_add_u32_e32 v238, v183, v251
	v_add_u32_e32 v239, v183, v252
	v_add_u32_e32 v240, v183, v250
	v_add_u32_e32 v241, v184, v251
	v_add_u32_e32 v242, v184, v252
	v_add_u32_e32 v243, v184, v250
	v_add_u32_e32 v244, v197, v251
	v_add_u32_e32 v245, v197, v252
	v_add_u32_e32 v246, v197, v250
	v_add_u32_e32 v247, v198, v251
	v_add_u32_e32 v248, v198, v252
	v_add_u32_e32 v249, v198, v250
	s_barrier

.LBB8_370:
	s_or_b64 exec, exec, s[34:35]
	s_waitcnt lgkmcnt(3)
	v_mfma_f32_32x32x16_f16 v[24:39], v[108:111], v[40:43], v[24:39]
	ds_read_b128 v[156:159], v187 offset:13728
	ds_read_b128 v[40:43], v189 offset:13728
	s_mov_b64 s[34:35], s[20:21]
	s_waitcnt vmcnt(1)
	ds_write_b128 v183, v[152:155] offset:63376
	s_waitcnt vmcnt(0)
	ds_write_b32 v238, v210 offset:63908
	s_waitcnt lgkmcnt(6)
	v_mfma_f32_32x32x16_f16 v[24:39], v[112:115], v[48:51], v[24:39]
	s_and_saveexec_b64 s[42:43], s[6:7]
	s_andn2_b64 s[34:35], s[20:21], exec
	s_and_b64 s[44:45], s[8:9], exec
	s_or_b64 s[34:35], s[34:35], s[44:45]
	ds_write_b32 v239, v210 offset:63896
	s_or_b64 exec, exec, s[42:43]
	s_and_saveexec_b64 s[42:43], s[34:35]
	ds_write_b32 v240, v210 offset:63920
	s_or_b64 exec, exec, s[42:43]
	s_waitcnt lgkmcnt(5)
	v_mfma_f32_32x32x16_f16 v[24:39], v[116:119], v[44:47], v[24:39]
	ds_read_b128 v[48:51], v187 offset:14784
	ds_read_b128 v[44:47], v189 offset:14784
	v_add_f32_e32 v211, v169, v20
	v_add_f32_e32 v212, v167, v21
	s_waitcnt lgkmcnt(6)
	v_mfma_f32_32x32x16_f16 v[24:39], v[120:123], v[160:163], v[24:39]
	s_and_saveexec_b64 s[34:35], s[12:13]
	s_xor_b64 s[34:35], exec, s[34:35]
	v_add_f32_e32 v212, v167, v21
	ds_write2st64_b32 v196, v211, v212 offset0:4 offset1:5
	s_andn2_saveexec_b64 s[34:35], s[34:35]
	s_or_b64 exec, exec, s[34:35]
	v_add_f32_e32 v214, v166, v22
	v_add_f32_e32 v213, v179, v23
	s_and_saveexec_b64 s[34:35], s[12:13]
	s_xor_b64 s[34:35], exec, s[34:35]
	v_add_f32_e32 v213, v179, v23
	ds_write2st64_b32 v196, v214, v213 offset0:6 offset1:7
	s_andn2_saveexec_b64 s[34:35], s[34:35]
	s_or_b64 exec, exec, s[34:35]
	s_waitcnt lgkmcnt(5)
	v_mfma_f32_32x32x16_f16 v[24:39], v[124:127], v[156:159], v[24:39]
	ds_read_b128 v[156:159], v187 offset:15840
	ds_read_b128 v[20:23], v189 offset:15840
	s_mov_b64 s[34:35], s[20:21]
	ds_write_b128 v184, v[4:7] offset:63376
	ds_write_b32 v241, v207 offset:63908
	s_waitcnt lgkmcnt(8)
	v_mfma_f32_32x32x16_f16 v[24:39], v[128:131], v[40:43], v[24:39]
	s_and_saveexec_b64 s[42:43], s[6:7]
	s_andn2_b64 s[34:35], s[20:21], exec
	s_and_b64 s[44:45], s[8:9], exec
	s_or_b64 s[34:35], s[34:35], s[44:45]
	ds_write_b32 v242, v207 offset:63896
	s_or_b64 exec, exec, s[42:43]
	s_and_saveexec_b64 s[42:43], s[34:35]
	ds_write_b32 v243, v207 offset:63920
	s_or_b64 exec, exec, s[42:43]
	s_waitcnt lgkmcnt(5)
	v_mfma_f32_32x32x16_f16 v[24:39], v[132:135], v[48:51], v[24:39]
	s_waitcnt lgkmcnt(4)
	v_mfma_f32_32x32x16_f16 v[24:39], v[136:139], v[44:47], v[24:39]
	s_and_saveexec_b64 s[34:35], s[2:3]
	s_cbranch_execz .LBB8_387
	s_mov_b64 s[44:45], s[20:21]
	ds_write_b128 v197, v[148:151] offset:63376
	ds_write_b32 v244, v208 offset:63908
	s_and_saveexec_b64 s[42:43], s[6:7]
	s_andn2_b64 s[44:45], s[20:21], exec
	s_and_b64 s[54:55], s[8:9], exec
	s_or_b64 s[44:45], s[44:45], s[54:55]
	ds_write_b32 v245, v208 offset:63896
	s_or_b64 exec, exec, s[42:43]
	s_and_b64 exec, exec, s[44:45]
	ds_write_b32 v246, v208 offset:63920
.LBB8_387:
	s_or_b64 exec, exec, s[34:35]
	s_waitcnt lgkmcnt(3)
	v_mfma_f32_32x32x16_f16 v[24:39], v[140:143], v[156:159], v[24:39]
	s_waitcnt lgkmcnt(2)
	v_mfma_f32_32x32x16_f16 v[24:39], v[144:147], v[20:23], v[24:39]
	s_and_saveexec_b64 s[34:35], s[4:5]
	s_cbranch_execz .LBB8_392
	s_mov_b64 s[44:45], s[20:21]
	ds_write_b128 v198, v[8:11] offset:63376
	ds_write_b32 v247, v209 offset:63908
	s_and_saveexec_b64 s[42:43], s[6:7]
	s_andn2_b64 s[44:45], s[20:21], exec
	s_and_b64 s[54:55], s[8:9], exec
	s_or_b64 s[44:45], s[44:45], s[54:55]
	ds_write_b32 v248, v209 offset:63896
	s_or_b64 exec, exec, s[42:43]
	s_and_b64 exec, exec, s[44:45]
	ds_write_b32 v249, v209 offset:63920

.LBB8_406:
	s_or_b64 exec, exec, s[14:15]
	s_waitcnt lgkmcnt(3)
	v_mfma_f32_32x32x16_f16 v[36:51], v[108:111], v[20:23], v[36:51]
	ds_read_b128 v[156:159], v188 offset:13728
	ds_read_b128 v[20:23], v200 offset:13728
	v_cndmask_b32_e64 v172, 0, 1, s[42:43]
	v_cmp_ne_u32_e64 s[14:15], 1, v172
	s_andn2_b64 vcc, exec, s[42:43]
	s_waitcnt lgkmcnt(4)
	v_mfma_f32_32x32x16_f16 v[36:51], v[112:115], v[168:171], v[36:51]
	s_cbranch_vccnz .LBB8_412
	s_mov_b64 s[38:39], s[20:21]
	s_waitcnt vmcnt(1)
	ds_write_b128 v183, v[152:155] offset:16
	s_waitcnt vmcnt(0)
	ds_write_b32 v238, v210 offset:548
	s_and_saveexec_b64 s[36:37], s[6:7]
	s_andn2_b64 s[38:39], s[20:21], exec
	s_and_b64 s[40:41], s[8:9], exec
	s_or_b64 s[38:39], s[38:39], s[40:41]
	ds_write_b32 v239, v210 offset:536
	s_or_b64 exec, exec, s[36:37]
	s_and_saveexec_b64 s[36:37], s[38:39]
	ds_write_b32 v240, v210 offset:560
	s_or_b64 exec, exec, s[36:37]
.LBB8_412:
	v_add_f32_e32 v17, v1, v17
	v_add_f32_e32 v0, v0, v16
	s_waitcnt lgkmcnt(3)
	v_mfma_f32_32x32x16_f16 v[36:51], v[116:119], v[160:163], v[36:51]
	ds_read_b128 v[160:163], v188 offset:14784
	s_waitcnt vmcnt(1)
	ds_read_b128 v[152:155], v200 offset:14784
	v_mov_b32_e32 v168, v32
	v_mov_b32_e32 v169, v12
	v_mov_b32_e32 v1, v28
	v_pk_add_f32 v[168:169], v[168:169], v[0:1]
	v_add_f32_e32 v176, v17, v33
	v_mov_b32_e32 v1, v25
	s_waitcnt lgkmcnt(4)
	v_mfma_f32_32x32x16_f16 v[36:51], v[120:123], v[164:167], v[36:51]
	s_and_saveexec_b64 s[36:37], s[12:13]
	s_xor_b64 s[36:37], exec, s[36:37]
	v_add_f32_e32 v176, v17, v33
	v_mov_b32_e32 v1, v25
	ds_write2st64_b32 v196, v168, v176 offset1:1
	s_andn2_saveexec_b64 s[36:37], s[36:37]
	s_or_b64 exec, exec, s[36:37]
	v_add_f32_e32 v0, v3, v19
	v_add_f32_e32 v2, v2, v18
	v_add_f32_e32 v178, v2, v34
	v_add_f32_e32 v177, v0, v35
	v_mov_b32_e32 v3, v27
	s_and_saveexec_b64 s[36:37], s[12:13]
	s_xor_b64 s[36:37], exec, s[36:37]
	v_add_f32_e32 v177, v0, v35
	v_mov_b32_e32 v3, v27
	ds_write2st64_b32 v196, v178, v177 offset0:2 offset1:3
	s_andn2_saveexec_b64 s[36:37], s[36:37]
	s_or_b64 exec, exec, s[36:37]
	s_waitcnt lgkmcnt(3)
	v_mfma_f32_32x32x16_f16 v[36:51], v[124:127], v[156:159], v[36:51]
	ds_read_b128 v[32:35], v188 offset:15840
	ds_read_b128 v[16:19], v200 offset:15840
	s_and_b64 vcc, exec, s[14:15]
	s_waitcnt lgkmcnt(4)
	v_mfma_f32_32x32x16_f16 v[36:51], v[128:131], v[20:23], v[36:51]
	s_cbranch_vccnz .LBB8_422
	s_mov_b64 s[36:37], s[20:21]
	ds_write_b128 v184, v[4:7] offset:16
	s_waitcnt vmcnt(0)
	ds_write_b32 v241, v207 offset:548
	s_and_saveexec_b64 s[14:15], s[6:7]
	s_andn2_b64 s[36:37], s[20:21], exec
	s_and_b64 s[38:39], s[8:9], exec
	s_or_b64 s[36:37], s[36:37], s[38:39]
	ds_write_b32 v242, v207 offset:536
	s_or_b64 exec, exec, s[14:15]
	s_and_saveexec_b64 s[14:15], s[36:37]
	ds_write_b32 v243, v207 offset:560
	s_or_b64 exec, exec, s[14:15]
.LBB8_422:
	s_waitcnt lgkmcnt(3)
	v_mfma_f32_32x32x16_f16 v[36:51], v[132:135], v[160:163], v[36:51]
	s_nor_b64 s[36:37], s[34:35], s[22:23]
	s_waitcnt lgkmcnt(2)
	v_mfma_f32_32x32x16_f16 v[36:51], v[136:139], v[152:155], v[36:51]
	s_and_saveexec_b64 s[14:15], s[36:37]
	s_cbranch_execz .LBB8_427
	s_mov_b64 s[38:39], s[20:21]
	ds_write_b128 v197, v[148:151] offset:16
	s_waitcnt vmcnt(0)
	ds_write_b32 v244, v208 offset:548
	s_and_saveexec_b64 s[36:37], s[6:7]
	s_andn2_b64 s[38:39], s[20:21], exec
	s_and_b64 s[40:41], s[8:9], exec
	s_or_b64 s[38:39], s[38:39], s[40:41]
	ds_write_b32 v245, v208 offset:536
	s_or_b64 exec, exec, s[36:37]
	s_and_b64 exec, exec, s[38:39]
	ds_write_b32 v246, v208 offset:560
.LBB8_427:
	s_or_b64 exec, exec, s[14:15]
	s_waitcnt lgkmcnt(1)
	v_mfma_f32_32x32x16_f16 v[36:51], v[140:143], v[32:35], v[36:51]
	s_nor_b64 s[34:35], s[34:35], s[26:27]
	s_waitcnt lgkmcnt(0)
	v_mfma_f32_32x32x16_f16 v[36:51], v[144:147], v[16:19], v[36:51]
	s_and_saveexec_b64 s[14:15], s[34:35]
	s_cbranch_execz .LBB8_432
	s_mov_b64 s[36:37], s[20:21]
	ds_write_b128 v198, v[8:11] offset:16
	s_waitcnt vmcnt(0)
	ds_write_b32 v247, v209 offset:548
	s_and_saveexec_b64 s[34:35], s[6:7]
	s_andn2_b64 s[36:37], s[20:21], exec
	s_and_b64 s[38:39], s[8:9], exec
	s_or_b64 s[36:37], s[36:37], s[38:39]
	ds_write_b32 v248, v209 offset:536
	s_or_b64 exec, exec, s[34:35]
	s_and_b64 exec, exec, s[36:37]
	ds_write_b32 v249, v209 offset:560

	.amdhsa_kernel _Z8k3t_mfmaILi1EEvPK15HIP_vector_typeIjLj4EEPKjS3_PKfPf
		.amdhsa_group_segment_fixed_size 0
		.amdhsa_private_segment_fixed_size 0
		.amdhsa_kernarg_size 296
		.amdhsa_user_sgpr_count 2
		.amdhsa_user_sgpr_dispatch_ptr 0
		.amdhsa_user_sgpr_queue_ptr 0
		.amdhsa_user_sgpr_kernarg_segment_ptr 1
		.amdhsa_user_sgpr_dispatch_id 0
		.amdhsa_user_sgpr_kernarg_preload_length 0
		.amdhsa_user_sgpr_kernarg_preload_offset 0
		.amdhsa_user_sgpr_private_segment_size 0
		.amdhsa_uses_dynamic_stack 0
		.amdhsa_enable_private_segment 0
		.amdhsa_system_sgpr_workgroup_id_x 1
		.amdhsa_system_sgpr_workgroup_id_y 0
		.amdhsa_system_sgpr_workgroup_id_z 0
		.amdhsa_system_sgpr_workgroup_info 0
		.amdhsa_system_vgpr_workitem_id 0
		.amdhsa_next_free_vgpr 254
		.amdhsa_next_free_sgpr 64
		.amdhsa_accum_offset 256
		.amdhsa_reserve_vcc 1
		.amdhsa_float_round_mode_32 0
		.amdhsa_float_round_mode_16_64 0
		.amdhsa_float_denorm_mode_32 3
		.amdhsa_float_denorm_mode_16_64 3
		.amdhsa_dx10_clamp 1
		.amdhsa_ieee_mode 1
		.amdhsa_fp16_overflow 0
		.amdhsa_tg_split 0
		.amdhsa_exception_fp_ieee_invalid_op 0
		.amdhsa_exception_fp_denorm_src 0
		.amdhsa_exception_fp_ieee_div_zero 0
		.amdhsa_exception_fp_ieee_overflow 0
		.amdhsa_exception_fp_ieee_underflow 0
		.amdhsa_exception_fp_ieee_inexact 0
		.amdhsa_exception_int_div_zero 0
	.end_amdhsa_kernel
	.text
.Lfunc_end8:
	.size	_Z8k3t_mfmaILi1EEvPK15HIP_vector_typeIjLj4EEPKjS3_PKfPf, .Lfunc_end8-_Z8k3t_mfmaILi1EEvPK15HIP_vector_typeIjLj4EEPKjS3_PKfPf
	.set _Z8k3t_mfmaILi1EEvPK15HIP_vector_typeIjLj4EEPKjS3_PKfPf.num_vgpr, 238
	.set _Z8k3t_mfmaILi1EEvPK15HIP_vector_typeIjLj4EEPKjS3_PKfPf.num_agpr, 0
	.set _Z8k3t_mfmaILi1EEvPK15HIP_vector_typeIjLj4EEPKjS3_PKfPf.numbered_sgpr, 64
	.set _Z8k3t_mfmaILi1EEvPK15HIP_vector_typeIjLj4EEPKjS3_PKfPf.num_named_barrier, 0
	.set _Z8k3t_mfmaILi1EEvPK15HIP_vector_typeIjLj4EEPKjS3_PKfPf.private_seg_size, 0
	.set _Z8k3t_mfmaILi1EEvPK15HIP_vector_typeIjLj4EEPKjS3_PKfPf.uses_vcc, 1
	.set _Z8k3t_mfmaILi1EEvPK15HIP_vector_typeIjLj4EEPKjS3_PKfPf.uses_flat_scratch, 0
	.set _Z8k3t_mfmaILi1EEvPK15HIP_vector_typeIjLj4EEPKjS3_PKfPf.has_dyn_sized_stack, 0
	.set _Z8k3t_mfmaILi1EEvPK15HIP_vector_typeIjLj4EEPKjS3_PKfPf.has_recursion, 0
	.set _Z8k3t_mfmaILi1EEvPK15HIP_vector_typeIjLj4EEPKjS3_PKfPf.has_indirect_call, 0

amdhsa.kernels:
  - .agpr_count:     0
    .args:
      - .actual_access:  read_only
        .address_space:  global
        .offset:         0
        .size:           8
        .value_kind:     global_buffer
      - .actual_access:  read_only
        .address_space:  global
        .offset:         8
        .size:           8
        .value_kind:     global_buffer
      - .actual_access:  read_only
        .address_space:  global
        .offset:         16
        .size:           8
        .value_kind:     global_buffer
      - .actual_access:  write_only
        .address_space:  global
        .offset:         24
        .size:           8
        .value_kind:     global_buffer
      - .actual_access:  write_only
        .address_space:  global
        .offset:         32
        .size:           8
        .value_kind:     global_buffer
    .group_segment_fixed_size: 6520
    .kernarg_segment_align: 8
    .kernarg_segment_size: 40
    .language:       OpenCL C
    .language_version:
      - 2
      - 0
    .max_flat_workgroup_size: 256
    .name:           _Z8k1_naivePKfS0_S0_P15HIP_vector_typeIjLj4EEPj
    .private_segment_fixed_size: 0
    .sgpr_count:     30
    .sgpr_spill_count: 0
    .symbol:         _Z8k1_naivePKfS0_S0_P15HIP_vector_typeIjLj4EEPj.kd
    .uniform_work_group_size: 1
    .uses_dynamic_stack: false
    .vgpr_count:     40
    .vgpr_spill_count: 0
    .wavefront_size: 64
  - .agpr_count:     0
    .args:
      - .actual_access:  read_only
        .address_space:  global
        .offset:         0
        .size:           8
        .value_kind:     global_buffer
      - .actual_access:  read_only
        .address_space:  global
        .offset:         8
        .size:           8
        .value_kind:     global_buffer
      - .actual_access:  read_only
        .address_space:  global
        .offset:         16
        .size:           8
        .value_kind:     global_buffer
      - .actual_access:  read_only
        .address_space:  global
        .offset:         24
        .size:           8
        .value_kind:     global_buffer
      - .actual_access:  write_only
        .address_space:  global
        .offset:         32
        .size:           8
        .value_kind:     global_buffer
      - .actual_access:  write_only
        .address_space:  global
        .offset:         40
        .size:           8
        .value_kind:     global_buffer
      - .offset:         48
        .size:           4
        .value_kind:     by_value
    .group_segment_fixed_size: 32448
    .kernarg_segment_align: 8
    .kernarg_segment_size: 52
    .language:       OpenCL C
    .language_version:
      - 2
      - 0
    .max_flat_workgroup_size: 256
    .name:           _Z8k2_naivePK15HIP_vector_typeIjLj4EEPKjPKfS6_PS0_Pji
    .private_segment_fixed_size: 0
    .sgpr_count:     30
    .sgpr_spill_count: 0
    .symbol:         _Z8k2_naivePK15HIP_vector_typeIjLj4EEPKjPKfS6_PS0_Pji.kd
    .uniform_work_group_size: 1
    .uses_dynamic_stack: false
    .vgpr_count:     102
    .vgpr_spill_count: 0
    .wavefront_size: 64
  - .agpr_count:     0
    .args:
      - .actual_access:  read_only
        .address_space:  global
        .offset:         0
        .size:           8
        .value_kind:     global_buffer
      - .actual_access:  read_only
        .address_space:  global
        .offset:         8
        .size:           8
        .value_kind:     global_buffer
      - .actual_access:  read_only
        .address_space:  global
        .offset:         16
        .size:           8
        .value_kind:     global_buffer
      - .actual_access:  read_only
        .address_space:  global
        .offset:         24
        .size:           8
        .value_kind:     global_buffer
      - .actual_access:  write_only
        .address_space:  global
        .offset:         32
        .size:           8
        .value_kind:     global_buffer
      - .actual_access:  write_only
        .address_space:  global
        .offset:         40
        .size:           8
        .value_kind:     global_buffer
      - .offset:         48
        .size:           4
        .value_kind:     hidden_block_count_x
      - .offset:         52
        .size:           4
        .value_kind:     hidden_block_count_y
      - .offset:         56
        .size:           4
        .value_kind:     hidden_block_count_z
      - .offset:         60
        .size:           2
        .value_kind:     hidden_group_size_x
      - .offset:         62
        .size:           2
        .value_kind:     hidden_group_size_y
      - .offset:         64
        .size:           2
        .value_kind:     hidden_group_size_z
      - .offset:         66
        .size:           2
        .value_kind:     hidden_remainder_x
      - .offset:         68
        .size:           2
        .value_kind:     hidden_remainder_y
      - .offset:         70
        .size:           2
        .value_kind:     hidden_remainder_z
      - .offset:         88
        .size:           8
        .value_kind:     hidden_global_offset_x
      - .offset:         96
        .size:           8
        .value_kind:     hidden_global_offset_y
      - .offset:         104
        .size:           8
        .value_kind:     hidden_global_offset_z
      - .offset:         112
        .size:           2
        .value_kind:     hidden_grid_dims
      - .offset:         168
        .size:           4
        .value_kind:     hidden_dynamic_lds_size
    .group_segment_fixed_size: 0
    .kernarg_segment_align: 8
    .kernarg_segment_size: 304
    .language:       OpenCL C
    .language_version:
      - 2
      - 0
    .max_flat_workgroup_size: 512
    .name:           _Z7k2_mfmaPK15HIP_vector_typeIjLj4EEPKjS2_PKfPS0_Pj
    .private_segment_fixed_size: 0
    .sgpr_count:     52
    .sgpr_spill_count: 0
    .symbol:         _Z7k2_mfmaPK15HIP_vector_typeIjLj4EEPKjS2_PKfPS0_Pj.kd
    .uniform_work_group_size: 1
    .uses_dynamic_stack: false
    .vgpr_count:     245
    .vgpr_spill_count: 0
    .wavefront_size: 64
  - .agpr_count:     0
    .args:
      - .actual_access:  read_only
        .address_space:  global
        .offset:         0
        .size:           8
        .value_kind:     global_buffer
      - .actual_access:  write_only
        .address_space:  global
        .offset:         8
        .size:           8
        .value_kind:     global_buffer
      - .offset:         16
        .size:           4
        .value_kind:     hidden_block_count_x
      - .offset:         20
        .size:           4
        .value_kind:     hidden_block_count_y
      - .offset:         24
        .size:           4
        .value_kind:     hidden_block_count_z
      - .offset:         28
        .size:           2
        .value_kind:     hidden_group_size_x
      - .offset:         30
        .size:           2
        .value_kind:     hidden_group_size_y
      - .offset:         32
        .size:           2
        .value_kind:     hidden_group_size_z
      - .offset:         34
        .size:           2
        .value_kind:     hidden_remainder_x
      - .offset:         36
        .size:           2
        .value_kind:     hidden_remainder_y
      - .offset:         38
        .size:           2
        .value_kind:     hidden_remainder_z
      - .offset:         56
        .size:           8
        .value_kind:     hidden_global_offset_x
      - .offset:         64
        .size:           8
        .value_kind:     hidden_global_offset_y
      - .offset:         72
        .size:           8
        .value_kind:     hidden_global_offset_z
      - .offset:         80
        .size:           2
        .value_kind:     hidden_grid_dims
    .group_segment_fixed_size: 0
    .kernarg_segment_align: 8
    .kernarg_segment_size: 272
    .language:       OpenCL C
    .language_version:
      - 2
      - 0
    .max_flat_workgroup_size: 1024
    .name:           _Z7prep_w3PKfP15HIP_vector_typeIjLj4EE
    .private_segment_fixed_size: 0
    .sgpr_count:     18
    .sgpr_spill_count: 0
    .symbol:         _Z7prep_w3PKfP15HIP_vector_typeIjLj4EE.kd
    .uniform_work_group_size: 1
    .uses_dynamic_stack: false
    .vgpr_count:     13
    .vgpr_spill_count: 0
    .wavefront_size: 64
  - .agpr_count:     0
    .args:
      - .actual_access:  read_only
        .address_space:  global
        .offset:         0
        .size:           8
        .value_kind:     global_buffer
      - .actual_access:  read_only
        .address_space:  global
        .offset:         8
        .size:           8
        .value_kind:     global_buffer
      - .actual_access:  read_only
        .address_space:  global
        .offset:         16
        .size:           8
        .value_kind:     global_buffer
      - .actual_access:  read_only
        .address_space:  global
        .offset:         24
        .size:           8
        .value_kind:     global_buffer
      - .address_space:  global
        .offset:         32
        .size:           8
        .value_kind:     global_buffer
      - .offset:         40
        .size:           4
        .value_kind:     by_value
      - .offset:         48
        .size:           4
        .value_kind:     hidden_block_count_x
      - .offset:         52
        .size:           4
        .value_kind:     hidden_block_count_y
      - .offset:         56
        .size:           4
        .value_kind:     hidden_block_count_z
      - .offset:         60
        .size:           2
        .value_kind:     hidden_group_size_x
      - .offset:         62
        .size:           2
        .value_kind:     hidden_group_size_y
      - .offset:         64
        .size:           2
        .value_kind:     hidden_group_size_z
      - .offset:         66
        .size:           2
        .value_kind:     hidden_remainder_x
      - .offset:         68
        .size:           2
        .value_kind:     hidden_remainder_y
      - .offset:         70
        .size:           2
        .value_kind:     hidden_remainder_z
      - .offset:         88
        .size:           8
        .value_kind:     hidden_global_offset_x
      - .offset:         96
        .size:           8
        .value_kind:     hidden_global_offset_y
      - .offset:         104
        .size:           8
        .value_kind:     hidden_global_offset_z
      - .offset:         112
        .size:           2
        .value_kind:     hidden_grid_dims
    .group_segment_fixed_size: 25344
    .kernarg_segment_align: 8
    .kernarg_segment_size: 304
    .language:       OpenCL C
    .language_version:
      - 2
      - 0
    .max_flat_workgroup_size: 64
    .name:           _Z7k3_mfmaPK15HIP_vector_typeIjLj4EEPKjS2_PKfPfi
    .private_segment_fixed_size: 0
    .sgpr_count:     52
    .sgpr_spill_count: 0
    .symbol:         _Z7k3_mfmaPK15HIP_vector_typeIjLj4EEPKjS2_PKfPfi.kd
    .uniform_work_group_size: 1
    .uses_dynamic_stack: false
    .vgpr_count:     192
    .vgpr_spill_count: 0
    .wavefront_size: 64
  - .agpr_count:     0
    .args:
      - .actual_access:  read_only
        .address_space:  global
        .offset:         0
        .size:           8
        .value_kind:     global_buffer
      - .actual_access:  read_only
        .address_space:  global
        .offset:         8
        .size:           8
        .value_kind:     global_buffer
      - .actual_access:  read_only
        .address_space:  global
        .offset:         16
        .size:           8
        .value_kind:     global_buffer
      - .actual_access:  write_only
        .address_space:  global
        .offset:         24
        .size:           8
        .value_kind:     global_buffer
      - .actual_access:  write_only
        .address_space:  global
        .offset:         32
        .size:           8
        .value_kind:     global_buffer
      - .actual_access:  read_only
        .address_space:  global
        .offset:         40
        .size:           8
        .value_kind:     global_buffer
      - .actual_access:  read_only
        .address_space:  global
        .offset:         48
        .size:           8
        .value_kind:     global_buffer
      - .actual_access:  read_only
        .address_space:  global
        .offset:         56
        .size:           8
        .value_kind:     global_buffer
      - .actual_access:  write_only
        .address_space:  global
        .offset:         64
        .size:           8
        .value_kind:     global_buffer
      - .actual_access:  write_only
        .address_space:  global
        .offset:         72
        .size:           8
        .value_kind:     global_buffer
    .group_segment_fixed_size: 62848
    .kernarg_segment_align: 8
    .kernarg_segment_size: 80
    .language:       OpenCL C
    .language_version:
      - 2
      - 0
    .max_flat_workgroup_size: 256
    .name:           _Z7k1_mfmaPKfS0_S0_P15HIP_vector_typeIjLj4EEPjS0_S0_S0_S3_S3_
    .private_segment_fixed_size: 0
    .sgpr_count:     28
    .sgpr_spill_count: 0
    .symbol:         _Z7k1_mfmaPKfS0_S0_P15HIP_vector_typeIjLj4EEPjS0_S0_S0_S3_S3_.kd
    .uniform_work_group_size: 1
    .uses_dynamic_stack: false
    .vgpr_count:     170
    .vgpr_spill_count: 0
    .wavefront_size: 64
  - .agpr_count:     0
    .args:
      - .actual_access:  read_only
        .address_space:  global
        .offset:         0
        .size:           8
        .value_kind:     global_buffer
      - .actual_access:  read_only
        .address_space:  global
        .offset:         8
        .size:           8
        .value_kind:     global_buffer
      - .actual_access:  read_only
        .address_space:  global
        .offset:         16
        .size:           8
        .value_kind:     global_buffer
      - .actual_access:  read_only
        .address_space:  global
        .offset:         24
        .size:           8
        .value_kind:     global_buffer
      - .actual_access:  write_only
        .address_space:  global
        .offset:         32
        .size:           8
        .value_kind:     global_buffer
      - .actual_access:  write_only
        .address_space:  global
        .offset:         40
        .size:           8
        .value_kind:     global_buffer
      - .actual_access:  read_only
        .address_space:  global
        .offset:         48
        .size:           8
        .value_kind:     global_buffer
      - .actual_access:  read_only
        .address_space:  global
        .offset:         56
        .size:           8
        .value_kind:     global_buffer
      - .actual_access:  read_only
        .address_space:  global
        .offset:         64
        .size:           8
        .value_kind:     global_buffer
      - .actual_access:  read_only
        .address_space:  global
        .offset:         72
        .size:           8
        .value_kind:     global_buffer
      - .actual_access:  write_only
        .address_space:  global
        .offset:         80
        .size:           8
        .value_kind:     global_buffer
    .group_segment_fixed_size: 0
    .kernarg_segment_align: 8
    .kernarg_segment_size: 88
    .language:       OpenCL C
    .language_version:
      - 2
      - 0
    .max_flat_workgroup_size: 512
    .name:           _Z8k23_mfmaPK15HIP_vector_typeIjLj4EEPKjS2_PKfPS0_PjS2_S4_S2_S6_Pf
    .private_segment_fixed_size: 0
    .sgpr_count:     72
    .sgpr_spill_count: 0
    .symbol:         _Z8k23_mfmaPK15HIP_vector_typeIjLj4EEPKjS2_PKfPS0_PjS2_S4_S2_S6_Pf.kd
    .uniform_work_group_size: 1
    .uses_dynamic_stack: false
    .vgpr_count:     230
    .vgpr_spill_count: 0
    .wavefront_size: 64
  - .agpr_count:     0
    .args:
      - .actual_access:  read_only
        .address_space:  global
        .offset:         0
        .size:           8
        .value_kind:     global_buffer
      - .actual_access:  read_only
        .address_space:  global
        .offset:         8
        .size:           8
        .value_kind:     global_buffer
      - .actual_access:  read_only
        .address_space:  global
        .offset:         16
        .size:           8
        .value_kind:     global_buffer
      - .actual_access:  read_only
        .address_space:  global
        .offset:         24
        .size:           8
        .value_kind:     global_buffer
      - .address_space:  global
        .offset:         32
        .size:           8
        .value_kind:     global_buffer
      - .offset:         40
        .size:           4
        .value_kind:     by_value
    .group_segment_fixed_size: 3240
    .kernarg_segment_align: 8
    .kernarg_segment_size: 44
    .language:       OpenCL C
    .language_version:
      - 2
      - 0
    .max_flat_workgroup_size: 256
    .name:           _Z8k3_naivePK15HIP_vector_typeIjLj4EEPKjPKfS6_Pfi
    .private_segment_fixed_size: 0
    .sgpr_count:     28
    .sgpr_spill_count: 0
    .symbol:         _Z8k3_naivePK15HIP_vector_typeIjLj4EEPKjPKfS6_Pfi.kd
    .uniform_work_group_size: 1
    .uses_dynamic_stack: false
    .vgpr_count:     32
    .vgpr_spill_count: 0
    .wavefront_size: 64
  - .agpr_count:     0
    .args:
      - .actual_access:  read_only
        .address_space:  global
        .offset:         0
        .size:           8
        .value_kind:     global_buffer
      - .actual_access:  read_only
        .address_space:  global
        .offset:         8
        .size:           8
        .value_kind:     global_buffer
      - .actual_access:  read_only
        .address_space:  global
        .offset:         16
        .size:           8
        .value_kind:     global_buffer
      - .actual_access:  read_only
        .address_space:  global
        .offset:         24
        .size:           8
        .value_kind:     global_buffer
      - .address_space:  global
        .offset:         32
        .size:           8
        .value_kind:     global_buffer
      - .offset:         40
        .size:           4
        .value_kind:     hidden_block_count_x
      - .offset:         44
        .size:           4
        .value_kind:     hidden_block_count_y
      - .offset:         48
        .size:           4
        .value_kind:     hidden_block_count_z
      - .offset:         52
        .size:           2
        .value_kind:     hidden_group_size_x
      - .offset:         54
        .size:           2
        .value_kind:     hidden_group_size_y
      - .offset:         56
        .size:           2
        .value_kind:     hidden_group_size_z
      - .offset:         58
        .size:           2
        .value_kind:     hidden_remainder_x
      - .offset:         60
        .size:           2
        .value_kind:     hidden_remainder_y
      - .offset:         62
        .size:           2
        .value_kind:     hidden_remainder_z
      - .offset:         80
        .size:           8
        .value_kind:     hidden_global_offset_x
      - .offset:         88
        .size:           8
        .value_kind:     hidden_global_offset_y
      - .offset:         96
        .size:           8
        .value_kind:     hidden_global_offset_z
      - .offset:         104
        .size:           2
        .value_kind:     hidden_grid_dims
      - .offset:         160
        .size:           4
        .value_kind:     hidden_dynamic_lds_size
    .group_segment_fixed_size: 0
    .kernarg_segment_align: 8
    .kernarg_segment_size: 296
    .language:       OpenCL C
    .language_version:
      - 2
      - 0
    .max_flat_workgroup_size: 512
    .name:           _Z8k3t_mfmaILi1EEvPK15HIP_vector_typeIjLj4EEPKjS3_PKfPf
    .private_segment_fixed_size: 0
    .sgpr_count:     70
    .sgpr_spill_count: 0
    .symbol:         _Z8k3t_mfmaILi1EEvPK15HIP_vector_typeIjLj4EEPKjS3_PKfPf.kd
    .uniform_work_group_size: 1
    .uses_dynamic_stack: false
    .vgpr_count:     254
    .vgpr_spill_count: 0
    .wavefront_size: 64
